# MoE GEMM phases: per-unit L2 round trips removed - expert counters cached in LDS for the unit scheduler and the gather, the unit bias block brought into LDS by LDS-DMA before the K-loop
# speedup vs baseline: 1.0116x; 1.0116x over previous
.LBB0_910:
	v_readlane_b32 s0, v254, 0
	s_cmp_lt_i32 s0, 11
	s_cselect_b64 s[16:17], -1, 0
	s_and_b64 s[0:1], s[16:17], s[6:7]
	s_andn2_b64 vcc, exec, s[0:1]
	s_cbranch_vccnz .LBB0_934
	s_mov_b64 s[6:7], s[78:79]
	s_waitcnt vmcnt(0) lgkmcnt(0)
	s_barrier
	s_load_dwordx2 s[18:19], s[6:7], 0xe0
	v_mov_b32_e32 v1, 0
	s_waitcnt lgkmcnt(0)
	global_load_dwordx4 v[2:5], v1, s[18:19]
	global_load_dwordx4 v[6:9], v1, s[18:19] offset:16
	global_load_dwordx4 v[10:13], v1, s[18:19] offset:32
	global_load_dwordx4 v[14:17], v1, s[18:19] offset:48
	global_load_dwordx4 v[18:21], v1, s[18:19] offset:64
	global_load_dwordx4 v[22:25], v1, s[18:19] offset:80
	global_load_dwordx4 v[26:29], v1, s[18:19] offset:96
	global_load_dwordx4 v[30:33], v1, s[18:19] offset:112
	s_mov_b32 m0, 0x20800
	v_and_b32_e32 v40, 63, v0
	v_lshlrev_b32_e32 v40, 2, v40
	global_load_lds_dword v40, s[18:19]
	s_abs_i32 s1, s74
	v_cvt_f32_u32_e32 v1, s1
	s_sub_i32 s0, 0, s1
	s_load_dwordx2 s[20:21], s[6:7], 0xb8
	v_rcp_iflag_f32_e32 v1, v1
	s_nop 0
	v_mul_f32_e32 v1, 0x4f7ffffe, v1
	v_cvt_u32_f32_e32 v1, v1
	s_nop 0
	v_readfirstlane_b32 s2, v1
	s_mul_i32 s3, s0, s2
	s_mul_hi_u32 s3, s2, s3
	s_add_i32 s2, s2, s3
	s_waitcnt vmcnt(7)
	v_add_u32_e32 v1, 0xff, v2
	v_add_u32_e32 v2, 0xff, v3
	v_add_u32_e32 v3, 0xff, v4
	v_ashrrev_i32_e32 v1, 8, v1
	v_ashrrev_i32_e32 v2, 8, v2
	v_add_u32_e32 v4, 0xff, v5
	v_ashrrev_i32_e32 v3, 8, v3
	v_add_u32_e32 v1, v2, v1
	s_waitcnt vmcnt(6)
	v_add_u32_e32 v5, 0xff, v6
	v_ashrrev_i32_e32 v4, 8, v4
	v_add_u32_e32 v1, v1, v3
	v_add_u32_e32 v6, 0xff, v7
	v_ashrrev_i32_e32 v5, 8, v5
	v_add_u32_e32 v1, v1, v4
	v_add_u32_e32 v7, 0xff, v8
	v_ashrrev_i32_e32 v6, 8, v6
	v_add_u32_e32 v1, v1, v5
	v_add_u32_e32 v8, 0xff, v9
	v_ashrrev_i32_e32 v7, 8, v7
	v_add_u32_e32 v1, v1, v6
	s_waitcnt vmcnt(5)
	v_add_u32_e32 v9, 0xff, v10
	v_ashrrev_i32_e32 v8, 8, v8
	v_add_u32_e32 v1, v1, v7
	v_add_u32_e32 v10, 0xff, v11
	v_ashrrev_i32_e32 v9, 8, v9
	v_add_u32_e32 v1, v1, v8
	v_add_u32_e32 v11, 0xff, v12
	v_ashrrev_i32_e32 v10, 8, v10
	v_add_u32_e32 v1, v1, v9
	v_add_u32_e32 v12, 0xff, v13
	v_ashrrev_i32_e32 v11, 8, v11
	v_add_u32_e32 v1, v1, v10
	s_waitcnt vmcnt(4)
	v_add_u32_e32 v13, 0xff, v14
	v_ashrrev_i32_e32 v12, 8, v12
	v_add_u32_e32 v1, v1, v11
	v_add_u32_e32 v14, 0xff, v15
	v_ashrrev_i32_e32 v13, 8, v13
	v_add_u32_e32 v1, v1, v12
	v_add_u32_e32 v15, 0xff, v16
	v_ashrrev_i32_e32 v14, 8, v14
	v_add_u32_e32 v1, v1, v13
	v_add_u32_e32 v16, 0xff, v17
	v_ashrrev_i32_e32 v15, 8, v15
	v_add_u32_e32 v1, v1, v14
	s_waitcnt vmcnt(3)
	v_add_u32_e32 v17, 0xff, v18
	v_ashrrev_i32_e32 v16, 8, v16
	v_add_u32_e32 v1, v1, v15
	v_add_u32_e32 v18, 0xff, v19
	v_ashrrev_i32_e32 v17, 8, v17
	v_add_u32_e32 v1, v1, v16
	v_add_u32_e32 v19, 0xff, v20
	v_ashrrev_i32_e32 v18, 8, v18
	v_add_u32_e32 v1, v1, v17
	v_add_u32_e32 v20, 0xff, v21
	v_ashrrev_i32_e32 v19, 8, v19
	v_add_u32_e32 v1, v1, v18
	s_waitcnt vmcnt(2)
	v_add_u32_e32 v21, 0xff, v22
	v_ashrrev_i32_e32 v20, 8, v20
	v_add_u32_e32 v1, v1, v19
	v_add_u32_e32 v22, 0xff, v23
	v_ashrrev_i32_e32 v21, 8, v21
	v_add_u32_e32 v1, v1, v20
	v_add_u32_e32 v23, 0xff, v24
	v_ashrrev_i32_e32 v22, 8, v22
	v_add_u32_e32 v1, v1, v21
	v_add_u32_e32 v24, 0xff, v25
	v_ashrrev_i32_e32 v23, 8, v23
	v_add_u32_e32 v1, v1, v22
	s_waitcnt vmcnt(1)
	v_add_u32_e32 v25, 0xff, v26
	v_ashrrev_i32_e32 v24, 8, v24
	v_add_u32_e32 v1, v1, v23
	v_add_u32_e32 v26, 0xff, v27
	v_ashrrev_i32_e32 v25, 8, v25
	v_add_u32_e32 v1, v1, v24
	v_add_u32_e32 v27, 0xff, v28
	v_ashrrev_i32_e32 v26, 8, v26
	v_add_u32_e32 v1, v1, v25
	v_add_u32_e32 v28, 0xff, v29
	v_ashrrev_i32_e32 v27, 8, v27
	v_add_u32_e32 v1, v1, v26
	s_waitcnt vmcnt(0)
	v_add_u32_e32 v29, 0xff, v30
	v_ashrrev_i32_e32 v28, 8, v28
	v_add_u32_e32 v1, v1, v27
	v_add_u32_e32 v30, 0xff, v31
	v_ashrrev_i32_e32 v29, 8, v29
	v_add_u32_e32 v1, v1, v28
	v_add_u32_e32 v31, 0xff, v32
	v_ashrrev_i32_e32 v30, 8, v30
	v_add_u32_e32 v1, v1, v29
	v_add_u32_e32 v32, 0xff, v33
	v_ashrrev_i32_e32 v31, 8, v31
	v_add_u32_e32 v1, v1, v30
	v_ashrrev_i32_e32 v32, 8, v32
	v_add_u32_e32 v1, v1, v31
	v_add_u32_e32 v1, v1, v32
	s_nop 0
	v_readfirstlane_b32 s0, v1
	s_lshl_b32 s14, s0, 4
	s_abs_i32 s4, s14
	s_mul_hi_u32 s2, s4, s2
	s_mul_i32 s2, s2, s1
	s_sub_i32 s2, s4, s2
	s_ashr_i32 s15, s14, 31
	s_sub_i32 s3, s2, s1
	s_cmp_ge_u32 s2, s1
	s_cselect_b32 s2, s3, s2
	s_sub_i32 s3, s2, s1
	s_cmp_ge_u32 s2, s1
	s_cselect_b32 s1, s3, s2
	s_xor_b32 s1, s1, s15
	s_sub_i32 s1, s1, s15
	s_cmp_lt_i32 s1, 1
	s_cselect_b64 s[2:3], -1, 0
	s_cmp_lt_i32 s90, s1
	s_cselect_b64 s[4:5], -1, 0
	s_or_b64 s[2:3], s[2:3], s[4:5]
	s_and_b64 vcc, exec, s[2:3]
	s_cbranch_vccnz .LBB0_915
	s_memrealtime s[4:5]
	s_memrealtime s[2:3]
	v_mov_b64_e32 v[2:3], 0x5db
	s_waitcnt lgkmcnt(0)
	s_sub_u32 s2, s2, s4
	s_subb_u32 s3, s3, s5
	v_cmp_gt_u64_e32 vcc, s[2:3], v[2:3]
	s_cbranch_vccnz .LBB0_915
	v_mov_b64_e32 v[2:3], 0x5dc

.LBB0_921:
	s_add_i32 s59, s59, 1
	s_mul_i32 s4, s59, s60
	s_mul_hi_u32 s5, s59, s74
	s_add_i32 s5, s5, s4
	s_mul_i32 s4, s59, s74
	s_add_u32 s4, s4, s90
	s_addc_u32 s5, s5, s1
	v_cmp_ge_i64_e32 vcc, s[4:5], v[168:169]
	v_cmp_lt_i64_e64 s[6:7], s[4:5], v[168:169]
	s_cbranch_vccnz .LBB0_923
	v_mov_b32_e32 v182, 0x20800
	ds_read_b128 v[6:9], v182
	ds_read_b128 v[10:13], v182 offset:16
	s_ashr_i32 s5, s4, 31
	s_lshr_b32 s5, s5, 29
	s_add_i32 s5, s4, s5
	s_ashr_i32 s8, s5, 3
	s_and_b32 s5, s5, -8
	s_sub_i32 s4, s4, s5
	v_mov_b32_e32 v2, s4
	v_alignbit_b32 v2, s0, v2, 31
	s_waitcnt lgkmcnt(0)
	v_add_u32_e32 v6, 0xff, v6
	v_readfirstlane_b32 s5, v2
	ds_read_b128 v[2:5], v182 offset:48
	ds_read_b128 v[14:17], v182 offset:32
	s_mul_i32 s4, s5, s4
	s_add_i32 s4, s4, s8
	s_ashr_i32 s5, s4, 31
	s_lshr_b32 s5, s5, 26
	s_add_i32 s5, s4, s5
	s_ashr_i32 s8, s5, 6
	s_lshl_b32 s8, s8, 2
	s_sub_i32 s9, s0, s8
	s_min_i32 s9, s9, 4
	s_abs_i32 s10, s9
	v_cvt_f32_u32_e32 v18, s10
	s_sub_i32 s12, 0, s10
	s_andn2_b32 s5, s5, 63
	s_sub_i32 s4, s4, s5
	v_rcp_iflag_f32_e32 v18, v18
	s_abs_i32 s5, s4
	s_xor_b32 s11, s4, s9
	s_ashr_i32 s11, s11, 31
	v_mul_f32_e32 v18, 0x4f7ffffe, v18
	v_cvt_u32_f32_e32 v18, v18
	v_ashrrev_i32_e32 v6, 8, v6
	v_add_u32_e32 v7, 0xff, v7
	v_add_u32_e32 v8, 0xff, v8
	v_readfirstlane_b32 s13, v18
	s_mul_i32 s12, s12, s13
	s_mul_hi_u32 s12, s13, s12
	s_add_i32 s13, s13, s12
	s_mul_hi_u32 s12, s5, s13
	s_mul_i32 s13, s12, s10
	s_sub_i32 s5, s5, s13
	s_add_i32 s14, s12, 1
	s_sub_i32 s13, s5, s10
	s_cmp_ge_u32 s5, s10
	s_cselect_b32 s12, s14, s12
	s_cselect_b32 s5, s13, s5
	s_add_i32 s13, s12, 1
	s_cmp_ge_u32 s5, s10
	s_cselect_b32 s5, s13, s12
	s_xor_b32 s5, s5, s11
	s_sub_i32 s38, s5, s11
	s_mul_i32 s5, s38, s9
	s_sub_i32 s4, s4, s5
	s_add_i32 s67, s4, s8
	s_cmp_gt_i32 s67, -1
	s_cselect_b64 s[4:5], -1, 0
	v_cmp_lt_i32_e32 vcc, s67, v6
	v_ashrrev_i32_e32 v7, 8, v7
	s_and_b64 s[4:5], s[4:5], vcc
	v_ashrrev_i32_e32 v8, 8, v8
	v_add_u32_e32 v7, v7, v6
	s_and_b64 s[4:5], s[4:5], exec
	v_add_u32_e32 v9, 0xff, v9
	v_cmp_ge_i32_e64 s[8:9], s67, v6
	v_cmp_lt_i32_e32 vcc, s67, v7
	v_add_u32_e32 v8, v8, v7
	s_cselect_b32 s4, s67, 0
	v_ashrrev_i32_e32 v9, 8, v9
	v_sub_u32_e32 v6, s67, v6
	v_cmp_ge_i32_e64 s[10:11], s67, v7
	v_cmp_lt_i32_e64 s[12:13], s67, v8
	s_and_b64 vcc, s[8:9], vcc
	v_mov_b32_e32 v19, s4
	v_add_u32_e32 v10, 0xff, v10
	v_sub_u32_e32 v7, s67, v7
	v_add_u32_e32 v9, v9, v8
	s_and_b64 s[10:11], s[10:11], s[12:13]
	v_cndmask_b32_e32 v6, v19, v6, vcc
	v_cmp_ge_i32_e64 s[14:15], s67, v8
	v_cndmask_b32_e64 v18, 0, 1, vcc
	v_cmp_lt_i32_e64 s[8:9], s67, v9
	v_cndmask_b32_e64 v6, v6, v7, s[10:11]
	v_ashrrev_i32_e32 v7, 8, v10
	v_sub_u32_e32 v8, s67, v8
	v_cndmask_b32_e64 v18, v18, 2, s[10:11]
	s_and_b64 vcc, s[14:15], s[8:9]
	v_add_u32_e32 v7, v7, v9
	v_cndmask_b32_e64 v18, v18, 3, vcc
	v_cndmask_b32_e32 v6, v6, v8, vcc
	v_cmp_ge_i32_e32 vcc, s67, v9
	v_cmp_lt_i32_e64 s[8:9], s67, v7
	v_sub_u32_e32 v8, s67, v9
	s_and_b64 vcc, vcc, s[8:9]
	v_cndmask_b32_e32 v6, v6, v8, vcc
	v_add_u32_e32 v8, 0xff, v11
	v_ashrrev_i32_e32 v8, 8, v8
	v_add_u32_e32 v8, v8, v7
	v_cndmask_b32_e64 v9, v18, 4, vcc
	v_cmp_ge_i32_e32 vcc, s67, v7
	v_cmp_lt_i32_e64 s[8:9], s67, v8
	v_sub_u32_e32 v7, s67, v7
	s_and_b64 vcc, vcc, s[8:9]
	v_cndmask_b32_e32 v6, v6, v7, vcc
	v_add_u32_e32 v7, 0xff, v12
	v_ashrrev_i32_e32 v7, 8, v7
	v_add_u32_e32 v18, v7, v8
	v_cndmask_b32_e64 v9, v9, 5, vcc
	v_cmp_ge_i32_e32 vcc, s67, v8
	v_cmp_lt_i32_e64 s[8:9], s67, v18
	v_sub_u32_e32 v7, s67, v8
	s_and_b64 vcc, vcc, s[8:9]
	v_cndmask_b32_e32 v20, v6, v7, vcc
	v_add_u32_e32 v6, 0xff, v13
	v_ashrrev_i32_e32 v6, 8, v6
	v_cndmask_b32_e64 v19, v9, 6, vcc
	v_add_u32_e32 v21, v6, v18
	ds_read_b128 v[6:9], v182 offset:80
	ds_read_b128 v[10:13], v182 offset:64
	s_waitcnt lgkmcnt(0)
	v_add_u32_e32 v14, 0xff, v14
	v_cmp_ge_i32_e32 vcc, s67, v18
	v_cmp_lt_i32_e64 s[8:9], s67, v21
	v_ashrrev_i32_e32 v14, 8, v14
	v_sub_u32_e32 v18, s67, v18
	s_and_b64 vcc, vcc, s[8:9]
	v_add_u32_e32 v14, v14, v21
	v_add_u32_e32 v15, 0xff, v15
	v_cndmask_b32_e64 v19, v19, 7, vcc
	v_cndmask_b32_e32 v18, v20, v18, vcc
	v_cmp_ge_i32_e32 vcc, s67, v21
	v_cmp_lt_i32_e64 s[8:9], s67, v14
	v_ashrrev_i32_e32 v15, 8, v15
	v_sub_u32_e32 v20, s67, v21
	s_and_b64 vcc, vcc, s[8:9]
	v_add_u32_e32 v15, v15, v14
	v_add_u32_e32 v16, 0xff, v16
	v_cndmask_b32_e64 v19, v19, 8, vcc
	v_cndmask_b32_e32 v18, v18, v20, vcc
	v_cmp_ge_i32_e32 vcc, s67, v14
	v_cmp_lt_i32_e64 s[8:9], s67, v15
	v_ashrrev_i32_e32 v16, 8, v16
	v_sub_u32_e32 v14, s67, v14
	s_and_b64 vcc, vcc, s[8:9]
	v_add_u32_e32 v16, v16, v15
	v_cndmask_b32_e64 v19, v19, 9, vcc
	v_cndmask_b32_e32 v14, v18, v14, vcc
	v_cmp_ge_i32_e32 vcc, s67, v15
	v_cmp_lt_i32_e64 s[8:9], s67, v16
	v_sub_u32_e32 v15, s67, v15
	s_and_b64 vcc, vcc, s[8:9]
	v_cndmask_b32_e32 v14, v14, v15, vcc
	v_add_u32_e32 v15, 0xff, v17
	v_ashrrev_i32_e32 v15, 8, v15
	v_add_u32_e32 v15, v15, v16
	v_add_u32_e32 v2, 0xff, v2
	v_cndmask_b32_e64 v18, v19, 10, vcc
	v_cmp_ge_i32_e32 vcc, s67, v16
	v_cmp_lt_i32_e64 s[8:9], s67, v15
	v_ashrrev_i32_e32 v2, 8, v2
	v_sub_u32_e32 v16, s67, v16
	s_and_b64 vcc, vcc, s[8:9]
	v_add_u32_e32 v2, v2, v15
	v_add_u32_e32 v3, 0xff, v3
	v_cndmask_b32_e64 v17, v18, 11, vcc
	v_cndmask_b32_e32 v14, v14, v16, vcc
	v_cmp_ge_i32_e32 vcc, s67, v15
	v_cmp_lt_i32_e64 s[8:9], s67, v2
	v_ashrrev_i32_e32 v3, 8, v3
	v_sub_u32_e32 v15, s67, v15
	s_and_b64 vcc, vcc, s[8:9]
	v_add_u32_e32 v3, v3, v2
	v_add_u32_e32 v4, 0xff, v4
	v_cndmask_b32_e64 v16, v17, 12, vcc
	v_cndmask_b32_e32 v14, v14, v15, vcc
	v_cmp_ge_i32_e32 vcc, s67, v2
	v_cmp_lt_i32_e64 s[8:9], s67, v3
	v_ashrrev_i32_e32 v4, 8, v4
	v_sub_u32_e32 v2, s67, v2
	s_and_b64 vcc, vcc, s[8:9]
	v_add_u32_e32 v18, v4, v3
	v_cndmask_b32_e64 v15, v16, 13, vcc
	v_cndmask_b32_e32 v2, v14, v2, vcc
	v_cmp_ge_i32_e32 vcc, s67, v3
	v_cmp_lt_i32_e64 s[8:9], s67, v18
	v_sub_u32_e32 v3, s67, v3
	s_and_b64 vcc, vcc, s[8:9]
	v_cndmask_b32_e32 v20, v2, v3, vcc
	v_add_u32_e32 v2, 0xff, v5
	v_cndmask_b32_e64 v19, v15, 14, vcc
	v_ashrrev_i32_e32 v21, 8, v2
	ds_read_b128 v[2:5], v182 offset:112
	ds_read_b128 v[14:17], v182 offset:96
	v_add_u32_e32 v21, v21, v18
	v_cmp_ge_i32_e32 vcc, s67, v18
	v_cmp_lt_i32_e64 s[8:9], s67, v21
	v_sub_u32_e32 v18, s67, v18
	s_and_b64 vcc, vcc, s[8:9]
	v_cndmask_b32_e64 v19, v19, 15, vcc
	v_cndmask_b32_e32 v18, v20, v18, vcc
	v_add_u32_e32 v10, 0xff, v10
	v_ashrrev_i32_e32 v10, 8, v10
	v_add_u32_e32 v10, v10, v21
	v_add_u32_e32 v11, 0xff, v11
	v_cmp_ge_i32_e32 vcc, s67, v21
	v_cmp_lt_i32_e64 s[8:9], s67, v10
	v_ashrrev_i32_e32 v11, 8, v11
	v_sub_u32_e32 v20, s67, v21
	s_and_b64 vcc, vcc, s[8:9]
	v_add_u32_e32 v11, v11, v10
	v_add_u32_e32 v12, 0xff, v12
	v_cndmask_b32_e64 v19, v19, 16, vcc
	v_cndmask_b32_e32 v18, v18, v20, vcc
	v_cmp_ge_i32_e32 vcc, s67, v10
	v_cmp_lt_i32_e64 s[8:9], s67, v11
	v_ashrrev_i32_e32 v12, 8, v12
	v_sub_u32_e32 v10, s67, v10
	s_and_b64 vcc, vcc, s[8:9]
	v_add_u32_e32 v12, v12, v11
	v_cndmask_b32_e64 v19, v19, 17, vcc
	v_cndmask_b32_e32 v10, v18, v10, vcc
	v_cmp_ge_i32_e32 vcc, s67, v11
	v_cmp_lt_i32_e64 s[8:9], s67, v12
	v_sub_u32_e32 v11, s67, v11
	s_and_b64 vcc, vcc, s[8:9]
	v_cndmask_b32_e32 v10, v10, v11, vcc
	v_add_u32_e32 v11, 0xff, v13
	v_ashrrev_i32_e32 v11, 8, v11
	v_add_u32_e32 v11, v11, v12
	v_add_u32_e32 v6, 0xff, v6
	v_cndmask_b32_e64 v18, v19, 18, vcc
	v_cmp_ge_i32_e32 vcc, s67, v12
	v_cmp_lt_i32_e64 s[8:9], s67, v11
	v_ashrrev_i32_e32 v6, 8, v6
	v_sub_u32_e32 v12, s67, v12
	s_and_b64 vcc, vcc, s[8:9]
	v_add_u32_e32 v6, v6, v11
	v_add_u32_e32 v7, 0xff, v7
	v_cndmask_b32_e64 v13, v18, 19, vcc
	v_cndmask_b32_e32 v10, v10, v12, vcc
	v_cmp_ge_i32_e32 vcc, s67, v11
	v_cmp_lt_i32_e64 s[8:9], s67, v6
	v_ashrrev_i32_e32 v7, 8, v7
	v_sub_u32_e32 v11, s67, v11
	s_and_b64 vcc, vcc, s[8:9]
	v_add_u32_e32 v7, v7, v6
	v_add_u32_e32 v8, 0xff, v8
	v_cndmask_b32_e64 v12, v13, 20, vcc
	v_cndmask_b32_e32 v10, v10, v11, vcc
	v_cmp_ge_i32_e32 vcc, s67, v6
	v_cmp_lt_i32_e64 s[8:9], s67, v7
	v_ashrrev_i32_e32 v8, 8, v8
	v_sub_u32_e32 v6, s67, v6
	s_and_b64 vcc, vcc, s[8:9]
	v_add_u32_e32 v8, v8, v7
	v_cndmask_b32_e64 v11, v12, 21, vcc
	v_cndmask_b32_e32 v6, v10, v6, vcc
	v_cmp_ge_i32_e32 vcc, s67, v7
	v_cmp_lt_i32_e64 s[8:9], s67, v8
	v_sub_u32_e32 v7, s67, v7
	s_and_b64 vcc, vcc, s[8:9]
	v_cndmask_b32_e32 v6, v6, v7, vcc
	v_add_u32_e32 v7, 0xff, v9
	v_ashrrev_i32_e32 v7, 8, v7
	v_add_u32_e32 v7, v7, v8
	v_cndmask_b32_e64 v10, v11, 22, vcc
	v_cmp_ge_i32_e32 vcc, s67, v8
	v_cmp_lt_i32_e64 s[8:9], s67, v7
	v_sub_u32_e32 v8, s67, v8
	s_and_b64 vcc, vcc, s[8:9]
	v_cndmask_b32_e32 v6, v6, v8, vcc
	v_cndmask_b32_e64 v9, v10, 23, vcc
	s_waitcnt lgkmcnt(0)
	v_add_u32_e32 v8, 0xff, v14
	v_ashrrev_i32_e32 v8, 8, v8
	v_add_u32_e32 v8, v8, v7
	v_cmp_ge_i32_e32 vcc, s67, v7
	v_cmp_lt_i32_e64 s[8:9], s67, v8
	v_sub_u32_e32 v7, s67, v7
	s_and_b64 vcc, vcc, s[8:9]
	v_cndmask_b32_e32 v6, v6, v7, vcc
	v_add_u32_e32 v7, 0xff, v15
	v_ashrrev_i32_e32 v7, 8, v7
	v_add_u32_e32 v7, v7, v8
	v_cndmask_b32_e64 v9, v9, 24, vcc
	v_cmp_ge_i32_e32 vcc, s67, v8
	v_cmp_lt_i32_e64 s[8:9], s67, v7
	v_sub_u32_e32 v8, s67, v8
	s_and_b64 vcc, vcc, s[8:9]
	v_cndmask_b32_e32 v6, v6, v8, vcc
	v_add_u32_e32 v8, 0xff, v16
	v_ashrrev_i32_e32 v8, 8, v8
	v_add_u32_e32 v8, v8, v7
	v_cndmask_b32_e64 v9, v9, 25, vcc
	v_cmp_ge_i32_e32 vcc, s67, v7
	v_cmp_lt_i32_e64 s[8:9], s67, v8
	v_sub_u32_e32 v7, s67, v7
	s_and_b64 vcc, vcc, s[8:9]
	v_cndmask_b32_e32 v6, v6, v7, vcc
	v_add_u32_e32 v7, 0xff, v17
	v_ashrrev_i32_e32 v7, 8, v7
	v_add_u32_e32 v7, v7, v8
	v_add_u32_e32 v2, 0xff, v2
	v_cndmask_b32_e64 v9, v9, 26, vcc
	v_cmp_ge_i32_e32 vcc, s67, v8
	v_cmp_lt_i32_e64 s[8:9], s67, v7
	v_ashrrev_i32_e32 v2, 8, v2
	v_sub_u32_e32 v8, s67, v8
	s_and_b64 vcc, vcc, s[8:9]
	v_add_u32_e32 v2, v2, v7
	v_add_u32_e32 v3, 0xff, v3
	v_cndmask_b32_e64 v9, v9, 27, vcc
	v_cndmask_b32_e32 v6, v6, v8, vcc
	v_cmp_ge_i32_e32 vcc, s67, v7
	v_cmp_lt_i32_e64 s[8:9], s67, v2
	v_ashrrev_i32_e32 v3, 8, v3
	v_sub_u32_e32 v7, s67, v7
	s_and_b64 vcc, vcc, s[8:9]
	v_add_u32_e32 v3, v3, v2
	v_add_u32_e32 v4, 0xff, v4
	v_cndmask_b32_e64 v8, v9, 28, vcc
	v_cndmask_b32_e32 v6, v6, v7, vcc
	v_cmp_ge_i32_e32 vcc, s67, v2
	v_cmp_lt_i32_e64 s[8:9], s67, v3
	v_ashrrev_i32_e32 v4, 8, v4
	v_sub_u32_e32 v2, s67, v2
	s_and_b64 vcc, vcc, s[8:9]
	v_add_u32_e32 v4, v4, v3
	v_cndmask_b32_e64 v7, v8, 29, vcc
	v_cndmask_b32_e32 v2, v6, v2, vcc
	v_cmp_ge_i32_e32 vcc, s67, v3
	v_cmp_lt_i32_e64 s[8:9], s67, v4
	v_sub_u32_e32 v3, s67, v3
	s_and_b64 vcc, vcc, s[8:9]
	v_cndmask_b32_e32 v2, v2, v3, vcc
	v_add_u32_e32 v3, 0xff, v5
	v_ashrrev_i32_e32 v3, 8, v3
	v_add_u32_e32 v3, v3, v4
	v_cndmask_b32_e64 v6, v7, 30, vcc
	v_cmp_ge_i32_e32 vcc, s67, v4
	v_cmp_lt_i32_e64 s[8:9], s67, v3
	v_sub_u32_e32 v3, s67, v4
	s_and_b64 vcc, vcc, s[8:9]
	v_cndmask_b32_e64 v4, v6, 31, vcc
	v_cndmask_b32_e32 v2, v2, v3, vcc
	v_readfirstlane_b32 s8, v4
	v_readfirstlane_b32 s68, v2
.LBB0_923:
	s_ashr_i32 s9, s8, 31
	s_ashr_i32 s39, s38, 31
	s_lshl_b64 s[4:5], s[38:39], 19
	s_lshl_b64 s[10:11], s[8:9], 23
	s_add_u32 s10, s37, s10
	s_addc_u32 s11, s50, s11
	s_add_u32 s10, s10, s4
	s_addc_u32 s11, s11, s5
	s_and_b64 s[4:5], s[6:7], exec
	s_cselect_b32 s4, s11, s45
	s_cselect_b32 s5, s10, s44
	s_lshl_b32 s39, s68, 8
	s_lshl_b64 s[14:15], s[8:9], 16
	s_or_b32 s43, s39, 0x80
	s_lshl_b64 s[12:13], s[8:9], 2
	s_add_u32 s12, s18, s12
	s_addc_u32 s13, s19, s13
	s_add_u32 s14, s41, s14
	s_addc_u32 s15, s51, s15
	s_add_u32 s9, s44, 0x100
	v_mov_b32_e32 v34, 0
	s_addc_u32 s69, s45, 0
	s_mov_b32 s70, -2
	s_mov_b64 s[44:45], s[30:31]
	v_mov_b32_e32 v35, v34
	v_mov_b32_e32 v36, v34
	v_mov_b32_e32 v37, v34
	v_mov_b32_e32 v42, v34
	v_mov_b32_e32 v43, v34
	v_mov_b32_e32 v44, v34
	v_mov_b32_e32 v45, v34
	v_mov_b32_e32 v50, v34
	v_mov_b32_e32 v51, v34
	v_mov_b32_e32 v52, v34
	v_mov_b32_e32 v53, v34
	v_mov_b32_e32 v58, v34
	v_mov_b32_e32 v59, v34
	v_mov_b32_e32 v60, v34
	v_mov_b32_e32 v61, v34
	v_mov_b32_e32 v66, v34
	v_mov_b32_e32 v67, v34
	v_mov_b32_e32 v68, v34
	v_mov_b32_e32 v69, v34
	v_mov_b32_e32 v74, v34
	v_mov_b32_e32 v75, v34
	v_mov_b32_e32 v76, v34
	v_mov_b32_e32 v77, v34
	v_mov_b32_e32 v82, v34
	v_mov_b32_e32 v83, v34
	v_mov_b32_e32 v84, v34
	v_mov_b32_e32 v85, v34
	v_mov_b32_e32 v90, v34
	v_mov_b32_e32 v91, v34
	v_mov_b32_e32 v92, v34
	v_mov_b32_e32 v93, v34
	v_mov_b32_e32 v38, v34
	v_mov_b32_e32 v39, v34
	v_mov_b32_e32 v40, v34
	v_mov_b32_e32 v41, v34
	v_mov_b32_e32 v46, v34
	v_mov_b32_e32 v47, v34
	v_mov_b32_e32 v48, v34
	v_mov_b32_e32 v49, v34
	v_mov_b32_e32 v54, v34
	v_mov_b32_e32 v55, v34
	v_mov_b32_e32 v56, v34
	v_mov_b32_e32 v57, v34
	v_mov_b32_e32 v62, v34
	v_mov_b32_e32 v63, v34
	v_mov_b32_e32 v64, v34
	v_mov_b32_e32 v65, v34
	v_mov_b32_e32 v70, v34
	v_mov_b32_e32 v71, v34
	v_mov_b32_e32 v72, v34
	v_mov_b32_e32 v73, v34
	v_mov_b32_e32 v78, v34
	v_mov_b32_e32 v79, v34
	v_mov_b32_e32 v80, v34
	v_mov_b32_e32 v81, v34
	v_mov_b32_e32 v86, v34
	v_mov_b32_e32 v87, v34
	v_mov_b32_e32 v88, v34
	v_mov_b32_e32 v89, v34
	v_mov_b32_e32 v94, v34
	v_mov_b32_e32 v95, v34
	v_mov_b32_e32 v96, v34
	v_mov_b32_e32 v97, v34
	v_mov_b32_e32 v98, v34
	v_mov_b32_e32 v99, v34
	v_mov_b32_e32 v100, v34
	v_mov_b32_e32 v101, v34
	v_mov_b32_e32 v106, v34
	v_mov_b32_e32 v107, v34
	v_mov_b32_e32 v108, v34
	v_mov_b32_e32 v109, v34
	v_mov_b32_e32 v114, v34
	v_mov_b32_e32 v115, v34
	v_mov_b32_e32 v116, v34
	v_mov_b32_e32 v117, v34
	v_mov_b32_e32 v122, v34
	v_mov_b32_e32 v123, v34
	v_mov_b32_e32 v124, v34
	v_mov_b32_e32 v125, v34
	v_mov_b32_e32 v130, v34
	v_mov_b32_e32 v131, v34
	v_mov_b32_e32 v132, v34
	v_mov_b32_e32 v133, v34
	v_mov_b32_e32 v138, v34
	v_mov_b32_e32 v139, v34
	v_mov_b32_e32 v140, v34
	v_mov_b32_e32 v141, v34
	v_mov_b32_e32 v146, v34
	v_mov_b32_e32 v147, v34
	v_mov_b32_e32 v148, v34
	v_mov_b32_e32 v149, v34
	v_mov_b32_e32 v150, v34
	v_mov_b32_e32 v151, v34
	v_mov_b32_e32 v152, v34
	v_mov_b32_e32 v153, v34
	v_mov_b32_e32 v102, v34
	v_mov_b32_e32 v103, v34
	v_mov_b32_e32 v104, v34
	v_mov_b32_e32 v105, v34
	v_mov_b32_e32 v110, v34
	v_mov_b32_e32 v111, v34
	v_mov_b32_e32 v112, v34
	v_mov_b32_e32 v113, v34
	v_mov_b32_e32 v118, v34
	v_mov_b32_e32 v119, v34
	v_mov_b32_e32 v120, v34
	v_mov_b32_e32 v121, v34
	v_mov_b32_e32 v126, v34
	v_mov_b32_e32 v127, v34
	v_mov_b32_e32 v128, v34
	v_mov_b32_e32 v129, v34
	v_mov_b32_e32 v134, v34
	v_mov_b32_e32 v135, v34
	v_mov_b32_e32 v136, v34
	v_mov_b32_e32 v137, v34
	v_mov_b32_e32 v142, v34
	v_mov_b32_e32 v143, v34
	v_mov_b32_e32 v144, v34
	v_mov_b32_e32 v145, v34
	v_mov_b32_e32 v154, v34
	v_mov_b32_e32 v155, v34
	v_mov_b32_e32 v156, v34
	v_mov_b32_e32 v157, v34
	v_mov_b32_e32 v158, v34
	v_mov_b32_e32 v159, v34
	v_mov_b32_e32 v160, v34
	v_mov_b32_e32 v161, v34
	v_readlane_b32 s46, v255, 30
	s_xor_b32 s46, s46, 1
	s_and_b32 s46, s46, 1
	v_writelane_b32 v255, s46, 30
	s_lshl_b32 s46, s46, 10
	s_add_u32 m0, s46, 0x20000
	s_lshl_b32 s48, s42, 14
	s_lshl_b32 s49, s40, 10
	s_add_u32 s48, s48, s49
	s_add_u32 s48, s20, s48
	s_addc_u32 s49, s21, 0
	v_and_b32_e32 v2, 63, v0
	v_lshlrev_b32_e32 v2, 4, v2
	global_load_lds_dwordx4 v2, s[48:49]
	s_branch .LBB0_926
.LBB0_924:
	v_mov_b32_e32 v165, v0
	s_sub_u32 s48, s12, s18
	s_add_u32 s48, s48, 0x20800
	v_mov_b32_e32 v166, s48
	ds_read_b32 v166, v166
	v_lshlrev_b32_e32 v167, 4, v165
	v_ashrrev_i32_e32 v170, 31, v165
	v_bfe_i32 v171, v165, 27, 1
	v_lshrrev_b32_e32 v170, 26, v170
	v_lshrrev_b32_e32 v171, 22, v171
	v_add_u32_e32 v172, 0x2000, v167
	v_add_u32_e32 v165, v165, v170
	v_add_u32_e32 v170, v167, v171
	v_ashrrev_i32_e32 v171, 31, v172
	v_and_b32_e32 v170, 0xfffffc00, v170
	v_lshrrev_b32_e32 v171, 22, v171
	v_sub_u32_e32 v167, v167, v170
	v_add_u32_e32 v171, v172, v171
	v_lshrrev_b32_e32 v173, 4, v167
	v_ashrrev_i32_e32 v174, 31, v167
	v_ashrrev_i32_e32 v181, 10, v171
	v_bitop3_b32 v182, v173, v167, 32 bitop3:0x6c
	v_lshrrev_b32_e32 v167, 26, v174
	v_mul_i32_i24_e32 v171, 0x400, v181
	v_add_u32_e32 v167, v182, v167
	v_sub_u32_e32 v171, v172, v171
	v_ashrrev_i32_e32 v183, 6, v167
	v_lshrrev_b32_e32 v167, 4, v171
	v_bitop3_b32 v184, v167, v171, 32 bitop3:0x6c
	v_ashrrev_i32_e32 v171, 31, v184
	v_ashrrev_i32_e32 v165, 6, v165
	v_lshrrev_b32_e32 v171, 26, v171
	v_lshlrev_b32_e32 v170, 3, v165
	v_lshlrev_b32_e32 v173, 3, v181
	v_add_u32_e32 v185, v184, v171
	v_and_b32_e32 v170, -16, v170
	v_and_b32_e32 v172, -16, v173
	v_ashrrev_i32_e32 v171, 6, v185
	v_add_u32_e32 v170, v183, v170
	v_add_u32_e32 v171, v171, v172
	v_add_u32_e32 v167, s39, v170
	v_add_u32_e32 v170, s43, v170
	v_add_u32_e32 v172, s39, v171
	v_add_u32_e32 v171, s43, v171
	v_lshlrev_b32_e32 v165, 5, v165
	v_and_b32_e32 v165, 32, v165
	s_waitcnt lgkmcnt(0)
	v_readfirstlane_b32 s48, v166
	s_add_i32 s48, s48, -1
	s_nop 0
	v_min_i32_e32 v166, s48, v167
	v_min_i32_e32 v170, s48, v170
	v_min_i32_e32 v172, s48, v172
	v_min_i32_e32 v174, s48, v171
	v_ashrrev_i32_e32 v167, 31, v166
	v_ashrrev_i32_e32 v171, 31, v170
	v_ashrrev_i32_e32 v173, 31, v172
	v_ashrrev_i32_e32 v175, 31, v174
	v_lshl_add_u64 v[166:167], v[166:167], 2, s[14:15]
	v_lshl_add_u64 v[170:171], v[170:171], 2, s[14:15]
	v_lshl_add_u64 v[172:173], v[172:173], 2, s[14:15]
	v_lshl_add_u64 v[174:175], v[174:175], 2, s[14:15]
	global_load_dword v166, v[166:167], off
	s_nop 0
	global_load_dword v170, v[170:171], off
	s_nop 0
	global_load_dword v171, v[172:173], off
	s_nop 0
	global_load_dword v172, v[174:175], off
	v_mul_i32_i24_e32 v174, 64, v183
	v_sub_u32_e32 v174, v182, v174
	v_ashrrev_i16_sdwa v174, v1, sext(v174) dst_sel:DWORD dst_unused:UNUSED_PAD src0_sel:DWORD src1_sel:BYTE_0
	v_bfe_i32 v174, v174, 0, 16
	v_add_lshl_u32 v165, v165, v174, 1
	v_and_b32_e32 v174, 0xc0, v185
	v_sub_u32_e32 v174, v184, v174
	v_lshlrev_b32_e32 v173, 5, v181
	v_ashrrev_i16_sdwa v174, v1, sext(v174) dst_sel:DWORD dst_unused:UNUSED_PAD src0_sel:DWORD src1_sel:BYTE_0
	v_and_b32_e32 v173, 32, v173
	v_bfe_i32 v174, v174, 0, 16
	v_add_lshl_u32 v173, v173, v174, 1
	v_mov_b32_e32 v167, v163
	s_waitcnt vmcnt(3)
	v_lshlrev_b32_e32 v166, 9, v166
	s_waitcnt vmcnt(2)
	v_lshlrev_b32_e32 v170, 9, v170
	s_waitcnt vmcnt(1)
	v_lshlrev_b32_e32 v171, 9, v171
	s_waitcnt vmcnt(0)
	v_lshlrev_b32_e32 v172, 9, v172
	v_and_b32_e32 v166, 0xfffff800, v166
	v_and_b32_e32 v174, 0xfffff800, v170
	v_and_b32_e32 v171, 0xfffff800, v171
	v_and_b32_e32 v175, 0xfffff800, v172
	v_add_u32_e32 v170, v165, v166
	v_add_u32_e32 v166, v165, v174
	v_add_u32_e32 v172, v173, v171
	v_add_u32_e32 v174, v173, v175

.LBB0_930:
	v_mov_b32_e32 v18, v0
	s_lshl_b32 s4, s40, 7
	v_readfirstlane_b32 s9, v18
	s_lshr_b32 s5, s9, 1
	s_and_b32 s5, s5, 0x60
	s_or_b32 s4, s5, s4
	v_lshrrev_b32_e32 v2, 1, v18
	s_ashr_i32 s43, s42, 31
	v_and_or_b32 v20, v2, 24, s4
	s_lshl_b64 s[4:5], s[42:43], 14
	s_add_u32 s4, s20, s4
	v_lshlrev_b32_e32 v2, 1, v20
	s_addc_u32 s5, s21, s5
	v_readlane_b32 s4, v255, 30
	s_and_b32 s4, s4, 1
	s_lshl_b32 s4, s4, 10
	s_add_u32 s4, s4, 0x20000
	v_lshlrev_b32_e32 v2, 2, v2
	v_and_b32_e32 v2, 0x3ff, v2
	v_add_u32_e32 v2, s4, v2
	ds_read_b128 v[14:17], v2
	ds_read_b128 v[10:13], v2 offset:16
	ds_read_b128 v[6:9], v2 offset:32
	ds_read_b128 v[2:5], v2 offset:48
	v_mov_b32_e32 v24, v163
	v_mov_b32_e32 v25, v163
	s_ashr_i32 s4, s9, 2
	s_andn2_b32 s4, s4, 63
	v_and_or_b32 v18, v18, 15, s4
	v_lshl_add_u32 v22, s2, 8, v18
	v_ashrrev_i32_e32 v23, 31, v22
	v_lshlrev_b64 v[18:19], 11, v[22:23]
	v_ashrrev_i32_e32 v21, 31, v20
	v_lshl_add_u64 v[18:19], s[26:27], 0, v[18:19]
	v_lshl_add_u64 v[18:19], v[18:19], 0, v[20:21]
	v_or_b32_e32 v26, 16, v22
	v_ashrrev_i32_e32 v27, 31, v26
	v_lshlrev_b64 v[26:27], 11, v[26:27]
	s_mov_b64 s[4:5], -1
	s_waitcnt lgkmcnt(0)
	v_mov_b32_e32 v28, v15
	v_mov_b32_e32 v29, v17
	v_mov_b32_e32 v15, v16
	v_pk_add_f32 v[16:17], v[28:29], 1.0 op_sel_hi:[1,0]
	v_pk_add_f32 v[28:29], v[158:159], v[14:15]
	v_mov_b32_e32 v32, v7
	v_mov_b32_e32 v33, v9
	v_mov_b32_e32 v182, v3
	v_mov_b32_e32 v7, v8
	v_mov_b32_e32 v3, v4
	v_min_f32_e32 v28, 0x40e00000, v28
	v_min_f32_e32 v29, 0x40e00000, v29
	v_pk_add_f32 v[8:9], v[32:33], 1.0 op_sel_hi:[1,0]
	v_pk_add_f32 v[32:33], v[154:155], v[6:7]
	v_pk_add_f32 v[154:155], v[156:157], v[2:3]
	v_pk_mul_f32 v[156:157], v[28:29], s[36:37] op_sel_hi:[1,0]
	v_mov_b32_e32 v30, v11
	v_mov_b32_e32 v31, v13
	v_mov_b32_e32 v11, v12
	v_exp_f32_e32 v156, v156
	v_exp_f32_e32 v157, v157
	v_pk_add_f32 v[12:13], v[30:31], 1.0 op_sel_hi:[1,0]
	v_pk_add_f32 v[30:31], v[160:161], v[10:11]
	v_min_f32_e32 v32, 0x40e00000, v32
	v_min_f32_e32 v30, 0x40e00000, v30
	v_min_f32_e32 v31, 0x40e00000, v31
	v_min_f32_e32 v33, 0x40e00000, v33
	v_pk_mul_f32 v[158:159], v[30:31], s[36:37] op_sel_hi:[1,0]
	v_pk_mul_f32 v[160:161], v[32:33], s[36:37] op_sel_hi:[1,0]
	v_exp_f32_e32 v158, v158
	v_exp_f32_e32 v159, v159
	v_exp_f32_e32 v160, v160
	v_exp_f32_e32 v161, v161
	v_pk_add_f32 v[156:157], v[156:157], 1.0 op_sel_hi:[1,0]
	v_mov_b32_e32 v183, v5
	v_rcp_f32_e32 v156, v156
	v_rcp_f32_e32 v157, v157
	v_min_f32_e32 v154, 0x40e00000, v154
	v_min_f32_e32 v155, 0x40e00000, v155
	v_pk_add_f32 v[4:5], v[182:183], 1.0 op_sel_hi:[1,0]
	v_pk_mul_f32 v[182:183], v[154:155], s[36:37] op_sel_hi:[1,0]
	v_pk_add_f32 v[150:151], v[150:151], v[16:17]
	v_exp_f32_e32 v182, v182
	v_exp_f32_e32 v183, v183
	v_pk_add_f32 v[158:159], v[158:159], 1.0 op_sel_hi:[1,0]
	v_pk_add_f32 v[160:161], v[160:161], 1.0 op_sel_hi:[1,0]
	v_med3_f32 v150, v150, s63, v180
	v_med3_f32 v151, v151, s63, v180
	v_rcp_f32_e32 v158, v158
	v_rcp_f32_e32 v159, v159
	v_rcp_f32_e32 v160, v160
	v_rcp_f32_e32 v161, v161
	v_pk_mul_f32 v[28:29], v[28:29], v[156:157]
	v_pk_add_f32 v[152:153], v[152:153], v[12:13]
	v_pk_mul_f32 v[28:29], v[150:151], v[28:29]
	v_pk_add_f32 v[146:147], v[146:147], v[8:9]
	v_cvt_pk_fp8_f32 v24, v28, v29
	v_pk_add_f32 v[182:183], v[182:183], 1.0 op_sel_hi:[1,0]
	v_pk_add_f32 v[142:143], v[142:143], v[14:15]
	v_med3_f32 v152, v152, s63, v180
	v_med3_f32 v153, v153, s63, v180
	v_med3_f32 v146, v146, s63, v180
	v_med3_f32 v147, v147, s63, v180
	v_rcp_f32_e32 v182, v182
	v_rcp_f32_e32 v183, v183
	v_pk_mul_f32 v[30:31], v[30:31], v[158:159]
	v_pk_mul_f32 v[32:33], v[32:33], v[160:161]
	v_min_f32_e32 v142, 0x40e00000, v142
	v_pk_mul_f32 v[32:33], v[146:147], v[32:33]
	v_pk_mul_f32 v[28:29], v[152:153], v[30:31]
	v_min_f32_e32 v143, 0x40e00000, v143
	v_cvt_pk_fp8_f32 v25, v32, v33
	v_cvt_pk_fp8_f32 v24, v28, v29 op_sel:[0,0,1]
	v_pk_mul_f32 v[28:29], v[142:143], s[36:37] op_sel_hi:[1,0]
	v_pk_add_f32 v[148:149], v[148:149], v[4:5]
	v_exp_f32_e32 v28, v28
	v_exp_f32_e32 v29, v29
	v_med3_f32 v148, v148, s63, v180
	v_med3_f32 v149, v149, s63, v180
	v_pk_mul_f32 v[154:155], v[154:155], v[182:183]
	v_pk_add_f32 v[28:29], v[28:29], 1.0 op_sel_hi:[1,0]
	v_pk_mul_f32 v[30:31], v[148:149], v[154:155]
	v_rcp_f32_e32 v28, v28
	v_cvt_pk_fp8_f32 v25, v30, v31 op_sel:[0,0,1]
	v_pk_add_f32 v[30:31], v[144:145], v[10:11]
	v_rcp_f32_e32 v29, v29
	v_min_f32_e32 v30, 0x40e00000, v30
	v_min_f32_e32 v31, 0x40e00000, v31
	v_pk_mul_f32 v[32:33], v[30:31], s[36:37] op_sel_hi:[1,0]
	global_store_dwordx2 v[18:19], v[24:25], off
	v_exp_f32_e32 v32, v32
	v_exp_f32_e32 v33, v33
	v_pk_add_f32 v[24:25], v[138:139], v[16:17]
	v_pk_mul_f32 v[28:29], v[142:143], v[28:29]
	v_med3_f32 v24, v24, s63, v180
	v_med3_f32 v25, v25, s63, v180
	v_pk_mul_f32 v[24:25], v[24:25], v[28:29]
	v_pk_add_f32 v[28:29], v[32:33], 1.0 op_sel_hi:[1,0]
	v_pk_add_f32 v[32:33], v[140:141], v[12:13]
	v_rcp_f32_e32 v28, v28
	v_rcp_f32_e32 v29, v29
	v_med3_f32 v32, v32, s63, v180
	v_med3_f32 v33, v33, s63, v180
	v_pk_add_f32 v[118:119], v[118:119], v[6:7]
	v_pk_mul_f32 v[28:29], v[30:31], v[28:29]
	v_pk_add_f32 v[30:31], v[134:135], v[6:7]
	v_pk_mul_f32 v[28:29], v[32:33], v[28:29]
	v_min_f32_e32 v30, 0x40e00000, v30
	v_min_f32_e32 v31, 0x40e00000, v31
	v_pk_mul_f32 v[134:135], v[30:31], s[36:37] op_sel_hi:[1,0]
	v_pk_add_f32 v[32:33], v[130:131], v[8:9]
	v_exp_f32_e32 v134, v134
	v_exp_f32_e32 v135, v135
	v_med3_f32 v32, v32, s63, v180
	v_med3_f32 v33, v33, s63, v180
	v_min_f32_e32 v118, 0x40e00000, v118
	v_pk_add_f32 v[130:131], v[134:135], 1.0 op_sel_hi:[1,0]
	v_pk_add_f32 v[134:135], v[136:137], v[2:3]
	v_rcp_f32_e32 v130, v130
	v_min_f32_e32 v134, 0x40e00000, v134
	v_min_f32_e32 v135, 0x40e00000, v135
	v_rcp_f32_e32 v131, v131
	v_pk_mul_f32 v[136:137], v[134:135], s[36:37] op_sel_hi:[1,0]
	v_min_f32_e32 v119, 0x40e00000, v119
	v_exp_f32_e32 v136, v136
	v_exp_f32_e32 v137, v137
	v_pk_mul_f32 v[30:31], v[30:31], v[130:131]
	v_pk_add_f32 v[130:131], v[132:133], v[4:5]
	v_pk_mul_f32 v[30:31], v[32:33], v[30:31]
	v_pk_add_f32 v[32:33], v[136:137], 1.0 op_sel_hi:[1,0]
	v_mov_b32_e32 v133, v163
	v_rcp_f32_e32 v32, v32
	v_rcp_f32_e32 v33, v33
	v_cvt_pk_fp8_f32 v133, v30, v31
	v_mov_b32_e32 v132, v163
	v_med3_f32 v130, v130, s63, v180
	v_med3_f32 v131, v131, s63, v180
	v_pk_mul_f32 v[32:33], v[134:135], v[32:33]
	v_cvt_pk_fp8_f32 v132, v24, v25
	v_pk_mul_f32 v[24:25], v[130:131], v[32:33]
	v_pk_add_f32 v[30:31], v[122:123], v[16:17]
	v_cvt_pk_fp8_f32 v133, v24, v25 op_sel:[0,0,1]
	v_lshl_add_u64 v[24:25], s[26:27], 0, v[26:27]
	v_pk_add_f32 v[26:27], v[126:127], v[14:15]
	v_cvt_pk_fp8_f32 v132, v28, v29 op_sel:[0,0,1]
	v_min_f32_e32 v26, 0x40e00000, v26
	v_min_f32_e32 v27, 0x40e00000, v27
	v_pk_mul_f32 v[28:29], v[26:27], s[36:37] op_sel_hi:[1,0]
	v_pk_mul_f32 v[122:123], v[118:119], s[36:37] op_sel_hi:[1,0]
	v_exp_f32_e32 v28, v28
	v_exp_f32_e32 v29, v29
	v_exp_f32_e32 v122, v122
	v_exp_f32_e32 v123, v123
	v_med3_f32 v30, v30, s63, v180
	v_pk_add_f32 v[28:29], v[28:29], 1.0 op_sel_hi:[1,0]
	v_med3_f32 v31, v31, s63, v180
	v_rcp_f32_e32 v28, v28
	v_rcp_f32_e32 v29, v29
	v_pk_add_f32 v[116:117], v[116:117], v[4:5]
	v_lshl_add_u64 v[24:25], v[24:25], 0, v[20:21]
	v_med3_f32 v116, v116, s63, v180
	v_pk_mul_f32 v[26:27], v[26:27], v[28:29]
	v_pk_add_f32 v[28:29], v[128:129], v[10:11]
	v_pk_mul_f32 v[26:27], v[30:31], v[26:27]
	v_min_f32_e32 v28, 0x40e00000, v28
	v_min_f32_e32 v29, 0x40e00000, v29
	v_pk_mul_f32 v[32:33], v[28:29], s[36:37] op_sel_hi:[1,0]
	v_pk_add_f32 v[30:31], v[124:125], v[12:13]
	v_exp_f32_e32 v32, v32
	v_exp_f32_e32 v33, v33
	v_med3_f32 v30, v30, s63, v180
	v_med3_f32 v31, v31, s63, v180
	v_med3_f32 v117, v117, s63, v180
	v_pk_add_f32 v[32:33], v[32:33], 1.0 op_sel_hi:[1,0]
	global_store_dwordx2 v[24:25], v[132:133], off
	v_rcp_f32_e32 v32, v32
	v_rcp_f32_e32 v33, v33
	v_or_b32_e32 v24, 32, v22
	v_ashrrev_i32_e32 v25, 31, v24
	v_lshlrev_b64 v[24:25], 11, v[24:25]
	v_pk_mul_f32 v[28:29], v[28:29], v[32:33]
	v_pk_add_f32 v[32:33], v[114:115], v[8:9]
	v_pk_mul_f32 v[28:29], v[30:31], v[28:29]
	v_pk_add_f32 v[30:31], v[122:123], 1.0 op_sel_hi:[1,0]
	v_med3_f32 v32, v32, s63, v180
	v_rcp_f32_e32 v30, v30
	v_rcp_f32_e32 v31, v31
	v_med3_f32 v33, v33, s63, v180
	v_lshl_add_u64 v[24:25], s[26:27], 0, v[24:25]
	v_lshl_add_u64 v[24:25], v[24:25], 0, v[20:21]
	v_pk_mul_f32 v[30:31], v[118:119], v[30:31]
	v_mov_b32_e32 v118, v163
	v_pk_mul_f32 v[30:31], v[32:33], v[30:31]
	v_pk_add_f32 v[32:33], v[120:121], v[2:3]
	v_mov_b32_e32 v119, v163
	v_min_f32_e32 v32, 0x40e00000, v32
	v_min_f32_e32 v33, 0x40e00000, v33
	v_pk_mul_f32 v[114:115], v[32:33], s[36:37] op_sel_hi:[1,0]
	v_cvt_pk_fp8_f32 v118, v26, v27
	v_exp_f32_e32 v114, v114
	v_exp_f32_e32 v115, v115
	v_cvt_pk_fp8_f32 v119, v30, v31
	v_cvt_pk_fp8_f32 v118, v28, v29 op_sel:[0,0,1]
	v_pk_add_f32 v[30:31], v[112:113], v[10:11]
	v_pk_add_f32 v[114:115], v[114:115], 1.0 op_sel_hi:[1,0]
	v_min_f32_e32 v30, 0x40e00000, v30
	v_rcp_f32_e32 v114, v114
	v_rcp_f32_e32 v115, v115
	v_min_f32_e32 v31, 0x40e00000, v31
	v_pk_add_f32 v[28:29], v[106:107], v[16:17]
	v_or_b32_e32 v22, 48, v22
	v_pk_mul_f32 v[26:27], v[32:33], v[114:115]
	v_pk_mul_f32 v[32:33], v[30:31], s[36:37] op_sel_hi:[1,0]
	v_pk_mul_f32 v[26:27], v[116:117], v[26:27]
	v_exp_f32_e32 v32, v32
	v_cvt_pk_fp8_f32 v119, v26, v27 op_sel:[0,0,1]
	v_exp_f32_e32 v33, v33
	v_med3_f32 v28, v28, s63, v180
	v_med3_f32 v29, v29, s63, v180
	global_store_dwordx2 v[24:25], v[118:119], off
	v_pk_add_f32 v[24:25], v[110:111], v[14:15]
	v_ashrrev_i32_e32 v23, 31, v22
	v_min_f32_e32 v24, 0x40e00000, v24
	v_min_f32_e32 v25, 0x40e00000, v25
	v_pk_mul_f32 v[26:27], v[24:25], s[36:37] op_sel_hi:[1,0]
	v_lshlrev_b64 v[22:23], 11, v[22:23]
	v_exp_f32_e32 v26, v26
	v_exp_f32_e32 v27, v27
	v_lshl_add_u64 v[22:23], s[26:27], 0, v[22:23]
	v_lshl_add_u64 v[20:21], v[22:23], 0, v[20:21]
	v_pk_add_f32 v[22:23], v[90:91], v[16:17]
	v_pk_add_f32 v[26:27], v[26:27], 1.0 op_sel_hi:[1,0]
	v_med3_f32 v22, v22, s63, v180
	v_rcp_f32_e32 v26, v26
	v_rcp_f32_e32 v27, v27
	v_med3_f32 v23, v23, s63, v180
	v_pk_mul_f32 v[24:25], v[24:25], v[26:27]
	v_pk_add_f32 v[26:27], v[32:33], 1.0 op_sel_hi:[1,0]
	v_pk_mul_f32 v[24:25], v[28:29], v[24:25]
	v_rcp_f32_e32 v26, v26
	v_rcp_f32_e32 v27, v27
	v_pk_add_f32 v[28:29], v[108:109], v[12:13]
	v_pk_mul_f32 v[26:27], v[30:31], v[26:27]
	v_pk_add_f32 v[30:31], v[102:103], v[6:7]
	v_med3_f32 v28, v28, s63, v180
	v_min_f32_e32 v30, 0x40e00000, v30
	v_min_f32_e32 v31, 0x40e00000, v31
	v_pk_mul_f32 v[32:33], v[30:31], s[36:37] op_sel_hi:[1,0]
	v_med3_f32 v29, v29, s63, v180
	v_exp_f32_e32 v32, v32
	v_exp_f32_e32 v33, v33
	v_pk_mul_f32 v[26:27], v[28:29], v[26:27]
	v_pk_add_f32 v[28:29], v[98:99], v[8:9]
	v_pk_add_f32 v[98:99], v[104:105], v[2:3]
	v_pk_add_f32 v[32:33], v[32:33], 1.0 op_sel_hi:[1,0]
	v_min_f32_e32 v98, 0x40e00000, v98
	v_min_f32_e32 v99, 0x40e00000, v99
	v_rcp_f32_e32 v32, v32
	v_rcp_f32_e32 v33, v33
	v_pk_mul_f32 v[102:103], v[98:99], s[36:37] op_sel_hi:[1,0]
	v_med3_f32 v28, v28, s63, v180
	v_exp_f32_e32 v102, v102
	v_exp_f32_e32 v103, v103
	v_med3_f32 v29, v29, s63, v180
	v_pk_mul_f32 v[30:31], v[30:31], v[32:33]
	v_pk_add_f32 v[32:33], v[100:101], v[4:5]
	v_pk_mul_f32 v[28:29], v[28:29], v[30:31]
	v_pk_add_f32 v[30:31], v[102:103], 1.0 op_sel_hi:[1,0]
	v_med3_f32 v32, v32, s63, v180
	v_rcp_f32_e32 v30, v30
	v_rcp_f32_e32 v31, v31
	v_med3_f32 v33, v33, s63, v180
	v_pk_mul_f32 v[30:31], v[98:99], v[30:31]
	v_mov_b32_e32 v99, v163
	v_cvt_pk_fp8_f32 v99, v28, v29
	v_mov_b32_e32 v98, v163
	v_cvt_pk_fp8_f32 v98, v24, v25
	v_pk_mul_f32 v[24:25], v[32:33], v[30:31]
	v_pk_add_f32 v[28:29], v[86:87], v[6:7]
	v_cvt_pk_fp8_f32 v99, v24, v25 op_sel:[0,0,1]
	v_pk_add_f32 v[24:25], v[94:95], v[14:15]
	v_cvt_pk_fp8_f32 v98, v26, v27 op_sel:[0,0,1]
	v_min_f32_e32 v24, 0x40e00000, v24
	v_min_f32_e32 v25, 0x40e00000, v25
	v_pk_mul_f32 v[26:27], v[24:25], s[36:37] op_sel_hi:[1,0]
	global_store_dwordx2 v[20:21], v[98:99], off
	v_exp_f32_e32 v26, v26
	v_exp_f32_e32 v27, v27
	v_min_f32_e32 v28, 0x40e00000, v28
	v_min_f32_e32 v29, 0x40e00000, v29
	v_pk_mul_f32 v[30:31], v[28:29], s[36:37] op_sel_hi:[1,0]
	v_pk_add_f32 v[20:21], v[26:27], 1.0 op_sel_hi:[1,0]
	v_exp_f32_e32 v30, v30
	v_rcp_f32_e32 v20, v20
	v_rcp_f32_e32 v21, v21
	v_exp_f32_e32 v31, v31
	v_mov_b32_e32 v33, v163
	v_mov_b32_e32 v32, v163
	v_pk_mul_f32 v[20:21], v[24:25], v[20:21]
	v_pk_add_f32 v[24:25], v[96:97], v[10:11]
	v_pk_mul_f32 v[20:21], v[22:23], v[20:21]
	v_min_f32_e32 v24, 0x40e00000, v24
	v_min_f32_e32 v25, 0x40e00000, v25
	v_pk_mul_f32 v[26:27], v[24:25], s[36:37] op_sel_hi:[1,0]
	v_pk_add_f32 v[22:23], v[92:93], v[12:13]
	v_exp_f32_e32 v26, v26
	v_exp_f32_e32 v27, v27
	v_med3_f32 v22, v22, s63, v180
	v_med3_f32 v23, v23, s63, v180
	v_cvt_pk_fp8_f32 v32, v20, v21
	v_pk_add_f32 v[26:27], v[26:27], 1.0 op_sel_hi:[1,0]
	s_nop 0
	v_rcp_f32_e32 v26, v26
	v_rcp_f32_e32 v27, v27
	s_nop 0
	v_pk_mul_f32 v[24:25], v[24:25], v[26:27]
	s_nop 0
	v_pk_mul_f32 v[22:23], v[22:23], v[24:25]
	v_pk_add_f32 v[24:25], v[30:31], 1.0 op_sel_hi:[1,0]
	v_pk_add_f32 v[26:27], v[82:83], v[8:9]
	v_rcp_f32_e32 v24, v24
	v_rcp_f32_e32 v25, v25
	v_med3_f32 v26, v26, s63, v180
	v_med3_f32 v27, v27, s63, v180
	v_pk_add_f32 v[30:31], v[84:85], v[4:5]
	v_pk_mul_f32 v[24:25], v[28:29], v[24:25]
	v_med3_f32 v30, v30, s63, v180
	v_pk_mul_f32 v[24:25], v[26:27], v[24:25]
	v_pk_add_f32 v[26:27], v[88:89], v[2:3]
	v_cvt_pk_fp8_f32 v33, v24, v25
	v_min_f32_e32 v26, 0x40e00000, v26
	v_min_f32_e32 v27, 0x40e00000, v27
	v_pk_mul_f32 v[28:29], v[26:27], s[36:37] op_sel_hi:[1,0]
	v_med3_f32 v31, v31, s63, v180
	v_exp_f32_e32 v28, v28
	v_exp_f32_e32 v29, v29
	v_cvt_pk_fp8_f32 v32, v22, v23 op_sel:[0,0,1]
	v_add_co_u32_e32 v24, vcc, s64, v18
	v_pk_add_f32 v[28:29], v[28:29], 1.0 op_sel_hi:[1,0]
	s_nop 0
	v_addc_co_u32_e32 v25, vcc, 0, v19, vcc
	v_rcp_f32_e32 v28, v28
	v_rcp_f32_e32 v29, v29
	s_nop 0
	v_pk_mul_f32 v[20:21], v[26:27], v[28:29]
	s_nop 0
	v_pk_mul_f32 v[20:21], v[30:31], v[20:21]
	v_pk_add_f32 v[28:29], v[70:71], v[6:7]
	v_cvt_pk_fp8_f32 v33, v20, v21 op_sel:[0,0,1]
	v_pk_add_f32 v[20:21], v[78:79], v[14:15]
	v_min_f32_e32 v28, 0x40e00000, v28
	v_min_f32_e32 v20, 0x40e00000, v20
	v_min_f32_e32 v21, 0x40e00000, v21
	v_pk_mul_f32 v[22:23], v[20:21], s[36:37] op_sel_hi:[1,0]
	v_min_f32_e32 v29, 0x40e00000, v29
	v_exp_f32_e32 v22, v22
	v_exp_f32_e32 v23, v23
	v_pk_mul_f32 v[30:31], v[28:29], s[36:37] op_sel_hi:[1,0]
	global_store_dwordx2 v[24:25], v[32:33], off
	v_pk_add_f32 v[24:25], v[74:75], v[16:17]
	v_pk_add_f32 v[22:23], v[22:23], 1.0 op_sel_hi:[1,0]
	v_exp_f32_e32 v30, v30
	v_rcp_f32_e32 v22, v22
	v_rcp_f32_e32 v23, v23
	v_exp_f32_e32 v31, v31
	v_med3_f32 v24, v24, s63, v180
	v_med3_f32 v25, v25, s63, v180
	v_pk_mul_f32 v[20:21], v[20:21], v[22:23]
	v_pk_add_f32 v[22:23], v[80:81], v[10:11]
	v_pk_mul_f32 v[20:21], v[24:25], v[20:21]
	v_min_f32_e32 v22, 0x40e00000, v22
	v_min_f32_e32 v23, 0x40e00000, v23
	v_pk_mul_f32 v[26:27], v[22:23], s[36:37] op_sel_hi:[1,0]
	v_pk_add_f32 v[24:25], v[76:77], v[12:13]
	v_exp_f32_e32 v26, v26
	v_exp_f32_e32 v27, v27
	v_med3_f32 v24, v24, s63, v180
	v_med3_f32 v25, v25, s63, v180
	v_mov_b32_e32 v33, v163
	v_pk_add_f32 v[26:27], v[26:27], 1.0 op_sel_hi:[1,0]
	v_mov_b32_e32 v32, v163
	v_rcp_f32_e32 v26, v26
	v_rcp_f32_e32 v27, v27
	v_cvt_pk_fp8_f32 v32, v20, v21
	v_pk_mul_f32 v[22:23], v[22:23], v[26:27]
	s_nop 0
	v_pk_mul_f32 v[22:23], v[24:25], v[22:23]
	v_pk_add_f32 v[24:25], v[30:31], 1.0 op_sel_hi:[1,0]
	v_pk_add_f32 v[26:27], v[66:67], v[8:9]
	v_rcp_f32_e32 v24, v24
	v_rcp_f32_e32 v25, v25
	v_med3_f32 v26, v26, s63, v180
	v_med3_f32 v27, v27, s63, v180
	v_pk_add_f32 v[30:31], v[68:69], v[4:5]
	v_pk_mul_f32 v[24:25], v[28:29], v[24:25]
	v_med3_f32 v30, v30, s63, v180
	v_pk_mul_f32 v[24:25], v[26:27], v[24:25]
	v_pk_add_f32 v[26:27], v[72:73], v[2:3]
	v_cvt_pk_fp8_f32 v33, v24, v25
	v_min_f32_e32 v26, 0x40e00000, v26
	v_min_f32_e32 v27, 0x40e00000, v27
	v_pk_mul_f32 v[28:29], v[26:27], s[36:37] op_sel_hi:[1,0]
	v_med3_f32 v31, v31, s63, v180
	v_exp_f32_e32 v28, v28
	v_exp_f32_e32 v29, v29
	v_cvt_pk_fp8_f32 v32, v22, v23 op_sel:[0,0,1]
	v_add_co_u32_e32 v24, vcc, s65, v18
	v_pk_add_f32 v[28:29], v[28:29], 1.0 op_sel_hi:[1,0]
	s_nop 0
	v_addc_co_u32_e32 v25, vcc, 0, v19, vcc
	v_rcp_f32_e32 v28, v28
	v_rcp_f32_e32 v29, v29
	s_nop 0
	v_pk_mul_f32 v[20:21], v[26:27], v[28:29]
	s_nop 0
	v_pk_mul_f32 v[20:21], v[30:31], v[20:21]
	v_pk_add_f32 v[28:29], v[54:55], v[6:7]
	v_cvt_pk_fp8_f32 v33, v20, v21 op_sel:[0,0,1]
	v_pk_add_f32 v[20:21], v[62:63], v[14:15]
	v_min_f32_e32 v28, 0x40e00000, v28
	v_min_f32_e32 v20, 0x40e00000, v20
	v_min_f32_e32 v21, 0x40e00000, v21
	v_pk_mul_f32 v[22:23], v[20:21], s[36:37] op_sel_hi:[1,0]
	v_min_f32_e32 v29, 0x40e00000, v29
	v_exp_f32_e32 v22, v22
	v_exp_f32_e32 v23, v23
	v_pk_mul_f32 v[30:31], v[28:29], s[36:37] op_sel_hi:[1,0]
	global_store_dwordx2 v[24:25], v[32:33], off
	v_pk_add_f32 v[24:25], v[58:59], v[16:17]
	v_pk_add_f32 v[22:23], v[22:23], 1.0 op_sel_hi:[1,0]
	v_exp_f32_e32 v30, v30
	v_rcp_f32_e32 v22, v22
	v_rcp_f32_e32 v23, v23
	v_exp_f32_e32 v31, v31
	v_med3_f32 v24, v24, s63, v180
	v_med3_f32 v25, v25, s63, v180
	v_pk_mul_f32 v[20:21], v[20:21], v[22:23]
	v_pk_add_f32 v[22:23], v[64:65], v[10:11]
	v_pk_mul_f32 v[20:21], v[24:25], v[20:21]
	v_min_f32_e32 v22, 0x40e00000, v22
	v_min_f32_e32 v23, 0x40e00000, v23
	v_pk_mul_f32 v[26:27], v[22:23], s[36:37] op_sel_hi:[1,0]
	v_pk_add_f32 v[24:25], v[60:61], v[12:13]
	v_exp_f32_e32 v26, v26
	v_exp_f32_e32 v27, v27
	v_med3_f32 v24, v24, s63, v180
	v_med3_f32 v25, v25, s63, v180
	v_mov_b32_e32 v33, v163
	v_pk_add_f32 v[26:27], v[26:27], 1.0 op_sel_hi:[1,0]
	v_mov_b32_e32 v32, v163
	v_rcp_f32_e32 v26, v26
	v_rcp_f32_e32 v27, v27
	v_cvt_pk_fp8_f32 v32, v20, v21
	v_pk_add_f32 v[14:15], v[46:47], v[14:15]
	v_pk_add_f32 v[10:11], v[48:49], v[10:11]
	v_pk_mul_f32 v[22:23], v[22:23], v[26:27]
	v_pk_add_f32 v[26:27], v[50:51], v[8:9]
	v_pk_mul_f32 v[22:23], v[24:25], v[22:23]
	v_pk_add_f32 v[24:25], v[30:31], 1.0 op_sel_hi:[1,0]
	v_med3_f32 v26, v26, s63, v180
	v_rcp_f32_e32 v24, v24
	v_rcp_f32_e32 v25, v25
	v_med3_f32 v27, v27, s63, v180
	v_pk_add_f32 v[30:31], v[52:53], v[4:5]
	v_min_f32_e32 v14, 0x40e00000, v14
	v_pk_mul_f32 v[24:25], v[28:29], v[24:25]
	v_med3_f32 v30, v30, s63, v180
	v_pk_mul_f32 v[24:25], v[26:27], v[24:25]
	v_pk_add_f32 v[26:27], v[56:57], v[2:3]
	v_cvt_pk_fp8_f32 v33, v24, v25
	v_min_f32_e32 v26, 0x40e00000, v26
	v_min_f32_e32 v27, 0x40e00000, v27
	v_pk_mul_f32 v[28:29], v[26:27], s[36:37] op_sel_hi:[1,0]
	v_med3_f32 v31, v31, s63, v180
	v_exp_f32_e32 v28, v28
	v_exp_f32_e32 v29, v29
	v_min_f32_e32 v15, 0x40e00000, v15
	v_min_f32_e32 v10, 0x40e00000, v10
	v_min_f32_e32 v11, 0x40e00000, v11
	v_pk_add_f32 v[28:29], v[28:29], 1.0 op_sel_hi:[1,0]
	v_pk_add_f32 v[16:17], v[42:43], v[16:17]
	v_rcp_f32_e32 v28, v28
	v_rcp_f32_e32 v29, v29
	v_med3_f32 v16, v16, s63, v180
	v_med3_f32 v17, v17, s63, v180
	v_pk_add_f32 v[6:7], v[38:39], v[6:7]
	v_pk_mul_f32 v[20:21], v[26:27], v[28:29]
	v_min_f32_e32 v6, 0x40e00000, v6
	v_pk_mul_f32 v[20:21], v[30:31], v[20:21]
	v_min_f32_e32 v7, 0x40e00000, v7
	v_cvt_pk_fp8_f32 v33, v20, v21 op_sel:[0,0,1]
	v_pk_mul_f32 v[20:21], v[14:15], s[36:37] op_sel_hi:[1,0]
	v_pk_add_f32 v[12:13], v[44:45], v[12:13]
	v_exp_f32_e32 v20, v20
	v_exp_f32_e32 v21, v21
	v_med3_f32 v12, v12, s63, v180
	v_med3_f32 v13, v13, s63, v180
	v_pk_add_f32 v[8:9], v[34:35], v[8:9]
	v_pk_add_f32 v[20:21], v[20:21], 1.0 op_sel_hi:[1,0]
	v_pk_add_f32 v[2:3], v[40:41], v[2:3]
	v_rcp_f32_e32 v20, v20
	v_rcp_f32_e32 v21, v21
	v_med3_f32 v8, v8, s63, v180
	v_med3_f32 v9, v9, s63, v180
	v_min_f32_e32 v2, 0x40e00000, v2
	v_pk_mul_f32 v[14:15], v[14:15], v[20:21]
	v_pk_mul_f32 v[20:21], v[10:11], s[36:37] op_sel_hi:[1,0]
	v_pk_mul_f32 v[14:15], v[16:17], v[14:15]
	v_exp_f32_e32 v20, v20
	v_exp_f32_e32 v21, v21
	v_min_f32_e32 v3, 0x40e00000, v3
	v_pk_add_f32 v[4:5], v[36:37], v[4:5]
	v_cvt_pk_fp8_f32 v32, v22, v23 op_sel:[0,0,1]
	v_pk_add_f32 v[16:17], v[20:21], 1.0 op_sel_hi:[1,0]
	v_pk_mul_f32 v[20:21], v[6:7], s[36:37] op_sel_hi:[1,0]
	v_rcp_f32_e32 v16, v16
	v_rcp_f32_e32 v17, v17
	v_exp_f32_e32 v20, v20
	v_exp_f32_e32 v21, v21
	v_med3_f32 v4, v4, s63, v180
	v_pk_mul_f32 v[10:11], v[10:11], v[16:17]
	v_med3_f32 v5, v5, s63, v180
	v_pk_mul_f32 v[10:11], v[12:13], v[10:11]
	v_pk_add_f32 v[12:13], v[20:21], 1.0 op_sel_hi:[1,0]
	v_add_co_u32_e32 v22, vcc, s66, v18
	v_rcp_f32_e32 v12, v12
	v_rcp_f32_e32 v13, v13
	v_addc_co_u32_e32 v23, vcc, 0, v19, vcc
	global_store_dwordx2 v[22:23], v[32:33], off
	v_pk_mul_f32 v[6:7], v[6:7], v[12:13]
	v_mov_b32_e32 v12, v163
	v_pk_mul_f32 v[6:7], v[8:9], v[6:7]
	v_pk_mul_f32 v[8:9], v[2:3], s[36:37] op_sel_hi:[1,0]
	v_mov_b32_e32 v13, v163
	v_exp_f32_e32 v8, v8
	v_exp_f32_e32 v9, v9
	v_cvt_pk_fp8_f32 v12, v14, v15
	v_cvt_pk_fp8_f32 v13, v6, v7
	v_pk_add_f32 v[8:9], v[8:9], 1.0 op_sel_hi:[1,0]
	s_nop 0
	v_rcp_f32_e32 v8, v8
	v_rcp_f32_e32 v9, v9
	v_cvt_pk_fp8_f32 v12, v10, v11 op_sel:[0,0,1]
	v_pk_mul_f32 v[2:3], v[2:3], v[8:9]
	s_nop 0
	v_pk_mul_f32 v[2:3], v[4:5], v[2:3]
	s_nop 0
	v_cvt_pk_fp8_f32 v13, v2, v3 op_sel:[0,0,1]
	v_add_co_u32_e32 v2, vcc, 0x58000, v18
	s_nop 1
	v_addc_co_u32_e32 v3, vcc, 0, v19, vcc
	s_andn2_b64 vcc, exec, s[6:7]
	global_store_dwordx2 v[2:3], v[12:13], off
	s_cbranch_vccnz .LBB0_920
	s_andn2_b64 vcc, exec, s[24:25]
	s_cbranch_vccnz .LBB0_919
	s_barrier
	s_branch .LBB0_919

.LBB0_979:
	v_readlane_b32 s0, v254, 0
	s_cmp_lt_i32 s0, 12
	s_cselect_b64 s[12:13], -1, 0
	s_and_b64 s[0:1], s[12:13], s[6:7]
	s_andn2_b64 vcc, exec, s[0:1]
	s_cbranch_vccnz .LBB0_1002
	s_mov_b64 s[6:7], s[78:79]
	s_waitcnt vmcnt(0) lgkmcnt(0)
	s_barrier
	s_load_dwordx2 s[14:15], s[6:7], 0xe0
	v_mov_b32_e32 v1, 0
	s_waitcnt lgkmcnt(0)
	global_load_dwordx4 v[2:5], v1, s[14:15]
	global_load_dwordx4 v[6:9], v1, s[14:15] offset:16
	global_load_dwordx4 v[10:13], v1, s[14:15] offset:32
	global_load_dwordx4 v[14:17], v1, s[14:15] offset:48
	global_load_dwordx4 v[18:21], v1, s[14:15] offset:64
	global_load_dwordx4 v[22:25], v1, s[14:15] offset:80
	global_load_dwordx4 v[26:29], v1, s[14:15] offset:96
	global_load_dwordx4 v[30:33], v1, s[14:15] offset:112
	s_mov_b32 m0, 0x20800
	v_and_b32_e32 v40, 63, v0
	v_lshlrev_b32_e32 v40, 2, v40
	global_load_lds_dword v40, s[14:15]
	s_abs_i32 s1, s74
	v_cvt_f32_u32_e32 v1, s1
	s_sub_i32 s0, 0, s1
	s_load_dwordx2 s[16:17], s[6:7], 0xc8
	v_rcp_iflag_f32_e32 v1, v1
	s_nop 0
	v_mul_f32_e32 v1, 0x4f7ffffe, v1
	v_cvt_u32_f32_e32 v1, v1
	s_nop 0
	v_readfirstlane_b32 s2, v1
	s_mul_i32 s3, s0, s2
	s_mul_hi_u32 s3, s2, s3
	s_add_i32 s2, s2, s3
	s_waitcnt vmcnt(7)
	v_add_u32_e32 v1, 0xff, v2
	v_add_u32_e32 v2, 0xff, v3
	v_add_u32_e32 v3, 0xff, v4
	v_ashrrev_i32_e32 v1, 8, v1
	v_ashrrev_i32_e32 v2, 8, v2
	v_add_u32_e32 v4, 0xff, v5
	v_ashrrev_i32_e32 v3, 8, v3
	v_add_u32_e32 v1, v2, v1
	s_waitcnt vmcnt(6)
	v_add_u32_e32 v5, 0xff, v6
	v_ashrrev_i32_e32 v4, 8, v4
	v_add_u32_e32 v1, v1, v3
	v_add_u32_e32 v6, 0xff, v7
	v_ashrrev_i32_e32 v5, 8, v5
	v_add_u32_e32 v1, v1, v4
	v_add_u32_e32 v7, 0xff, v8
	v_ashrrev_i32_e32 v6, 8, v6
	v_add_u32_e32 v1, v1, v5
	v_add_u32_e32 v8, 0xff, v9
	v_ashrrev_i32_e32 v7, 8, v7
	v_add_u32_e32 v1, v1, v6
	s_waitcnt vmcnt(5)
	v_add_u32_e32 v9, 0xff, v10
	v_ashrrev_i32_e32 v8, 8, v8
	v_add_u32_e32 v1, v1, v7
	v_add_u32_e32 v10, 0xff, v11
	v_ashrrev_i32_e32 v9, 8, v9
	v_add_u32_e32 v1, v1, v8
	v_add_u32_e32 v11, 0xff, v12
	v_ashrrev_i32_e32 v10, 8, v10
	v_add_u32_e32 v1, v1, v9
	v_add_u32_e32 v12, 0xff, v13
	v_ashrrev_i32_e32 v11, 8, v11
	v_add_u32_e32 v1, v1, v10
	s_waitcnt vmcnt(4)
	v_add_u32_e32 v13, 0xff, v14
	v_ashrrev_i32_e32 v12, 8, v12
	v_add_u32_e32 v1, v1, v11
	v_add_u32_e32 v14, 0xff, v15
	v_ashrrev_i32_e32 v13, 8, v13
	v_add_u32_e32 v1, v1, v12
	v_add_u32_e32 v15, 0xff, v16
	v_ashrrev_i32_e32 v14, 8, v14
	v_add_u32_e32 v1, v1, v13
	v_add_u32_e32 v16, 0xff, v17
	v_ashrrev_i32_e32 v15, 8, v15
	v_add_u32_e32 v1, v1, v14
	s_waitcnt vmcnt(3)
	v_add_u32_e32 v17, 0xff, v18
	v_ashrrev_i32_e32 v16, 8, v16
	v_add_u32_e32 v1, v1, v15
	v_add_u32_e32 v18, 0xff, v19
	v_ashrrev_i32_e32 v17, 8, v17
	v_add_u32_e32 v1, v1, v16
	v_add_u32_e32 v19, 0xff, v20
	v_ashrrev_i32_e32 v18, 8, v18
	v_add_u32_e32 v1, v1, v17
	v_add_u32_e32 v20, 0xff, v21
	v_ashrrev_i32_e32 v19, 8, v19
	v_add_u32_e32 v1, v1, v18
	s_waitcnt vmcnt(2)
	v_add_u32_e32 v21, 0xff, v22
	v_ashrrev_i32_e32 v20, 8, v20
	v_add_u32_e32 v1, v1, v19
	v_add_u32_e32 v22, 0xff, v23
	v_ashrrev_i32_e32 v21, 8, v21
	v_add_u32_e32 v1, v1, v20
	v_add_u32_e32 v23, 0xff, v24
	v_ashrrev_i32_e32 v22, 8, v22
	v_add_u32_e32 v1, v1, v21
	v_add_u32_e32 v24, 0xff, v25
	v_ashrrev_i32_e32 v23, 8, v23
	v_add_u32_e32 v1, v1, v22
	s_waitcnt vmcnt(1)
	v_add_u32_e32 v25, 0xff, v26
	v_ashrrev_i32_e32 v24, 8, v24
	v_add_u32_e32 v1, v1, v23
	v_add_u32_e32 v26, 0xff, v27
	v_ashrrev_i32_e32 v25, 8, v25
	v_add_u32_e32 v1, v1, v24
	v_add_u32_e32 v27, 0xff, v28
	v_ashrrev_i32_e32 v26, 8, v26
	v_add_u32_e32 v1, v1, v25
	v_add_u32_e32 v28, 0xff, v29
	v_ashrrev_i32_e32 v27, 8, v27
	v_add_u32_e32 v1, v1, v26
	s_waitcnt vmcnt(0)
	v_add_u32_e32 v29, 0xff, v30
	v_ashrrev_i32_e32 v28, 8, v28
	v_add_u32_e32 v1, v1, v27
	v_add_u32_e32 v30, 0xff, v31
	v_ashrrev_i32_e32 v29, 8, v29
	v_add_u32_e32 v1, v1, v28
	v_add_u32_e32 v31, 0xff, v32
	v_ashrrev_i32_e32 v30, 8, v30
	v_add_u32_e32 v1, v1, v29
	v_add_u32_e32 v32, 0xff, v33
	v_ashrrev_i32_e32 v31, 8, v31
	v_add_u32_e32 v1, v1, v30
	v_ashrrev_i32_e32 v32, 8, v32
	v_add_u32_e32 v1, v1, v31
	v_add_u32_e32 v1, v1, v32
	s_nop 0
	v_readfirstlane_b32 s0, v1
	s_lshl_b32 s8, s0, 3
	s_abs_i32 s4, s8
	s_mul_hi_u32 s2, s4, s2
	s_mul_i32 s2, s2, s1
	s_sub_i32 s2, s4, s2
	s_ashr_i32 s9, s8, 31
	s_sub_i32 s3, s2, s1
	s_cmp_ge_u32 s2, s1
	s_cselect_b32 s2, s3, s2
	s_sub_i32 s3, s2, s1
	s_cmp_ge_u32 s2, s1
	s_cselect_b32 s1, s3, s2
	s_xor_b32 s1, s1, s9
	s_sub_i32 s1, s1, s9
	s_cmp_lt_i32 s1, 1
	s_cselect_b64 s[2:3], -1, 0
	s_cmp_lt_i32 s90, s1
	s_cselect_b64 s[4:5], -1, 0
	s_or_b64 s[2:3], s[2:3], s[4:5]
	s_and_b64 vcc, exec, s[2:3]
	s_cbranch_vccnz .LBB0_984
	s_memrealtime s[4:5]
	s_memrealtime s[2:3]
	v_mov_b64_e32 v[2:3], 0x5db
	s_waitcnt lgkmcnt(0)
	s_sub_u32 s2, s2, s4
	s_subb_u32 s3, s3, s5
	v_cmp_gt_u64_e32 vcc, s[2:3], v[2:3]
	s_cbranch_vccnz .LBB0_984
	v_mov_b64_e32 v[2:3], 0x5dc

.LBB0_990:
	s_add_i32 s54, s54, 1
	s_mul_i32 s4, s54, s56
	s_mul_hi_u32 s5, s54, s74
	s_add_i32 s5, s5, s4
	s_mul_i32 s4, s54, s74
	s_add_u32 s4, s4, s90
	s_addc_u32 s5, s5, s1
	v_cmp_ge_i64_e32 vcc, s[4:5], v[174:175]
	v_cmp_lt_i64_e64 s[6:7], s[4:5], v[174:175]
	s_cbranch_vccnz .LBB0_992
	v_mov_b32_e32 v182, 0x20800
	ds_read_b128 v[2:5], v182
	ds_read_b128 v[6:9], v182 offset:16
	ds_read_b128 v[10:13], v182 offset:48
	ds_read_b128 v[14:17], v182 offset:32
	ds_read_b128 v[18:21], v182 offset:80
	ds_read_b128 v[22:25], v182 offset:64
	s_ashr_i32 s5, s4, 31
	s_lshr_b32 s5, s5, 29
	s_add_i32 s5, s4, s5
	s_ashr_i32 s8, s5, 3
	s_and_b32 s5, s5, -8
	s_sub_i32 s4, s4, s5
	s_lshr_b32 s5, s4, 31
	s_add_i32 s5, s5, s0
	s_mul_i32 s4, s5, s4
	s_add_i32 s4, s4, s8
	s_ashr_i32 s5, s4, 31
	s_lshr_b32 s5, s5, 27
	s_add_i32 s5, s4, s5
	s_ashr_i32 s8, s5, 5
	s_lshl_b32 s8, s8, 2
	s_sub_i32 s9, s0, s8
	s_min_i32 s9, s9, 4
	s_abs_i32 s10, s9
	v_cvt_f32_u32_e32 v26, s10
	s_sub_i32 s30, 0, s10
	s_andn2_b32 s5, s5, 31
	s_sub_i32 s4, s4, s5
	v_rcp_iflag_f32_e32 v26, v26
	s_abs_i32 s5, s4
	s_xor_b32 s11, s4, s9
	s_ashr_i32 s11, s11, 31
	v_mul_f32_e32 v26, 0x4f7ffffe, v26
	v_cvt_u32_f32_e32 v26, v26
	s_waitcnt lgkmcnt(0)
	v_add_u32_e32 v11, 0xff, v11
	v_readfirstlane_b32 s31, v26
	s_mul_i32 s30, s30, s31
	s_mul_hi_u32 s30, s31, s30
	s_add_i32 s31, s31, s30
	s_mul_hi_u32 s30, s5, s31
	s_mul_i32 s31, s30, s10
	s_sub_i32 s5, s5, s31
	s_add_i32 s34, s30, 1
	s_sub_i32 s31, s5, s10
	s_cmp_ge_u32 s5, s10
	s_cselect_b32 s30, s34, s30
	s_cselect_b32 s5, s31, s5
	s_add_i32 s31, s30, 1
	s_cmp_ge_u32 s5, s10
	s_cselect_b32 s5, s31, s30
	s_xor_b32 s5, s5, s11
	s_sub_i32 s30, s5, s11
	s_mul_i32 s5, s30, s9
	s_sub_i32 s4, s4, s5
	v_add_u32_e32 v2, 0xff, v2
	v_add_u32_e32 v3, 0xff, v3
	s_add_i32 s34, s4, s8
	v_add_u32_e32 v4, 0xff, v4
	v_ashrrev_i32_e32 v3, 8, v3
	v_ashrrev_i32_e32 v2, 8, v2
	v_add_u32_e32 v5, 0xff, v5
	v_ashrrev_i32_e32 v4, 8, v4
	v_cmp_ge_i32_e32 vcc, s34, v2
	v_add_u32_e32 v2, v3, v2
	v_add_u32_e32 v6, 0xff, v6
	v_ashrrev_i32_e32 v5, 8, v5
	v_cmp_lt_i32_e64 s[8:9], s34, v2
	v_cmp_ge_i32_e64 s[10:11], s34, v2
	v_add_u32_e32 v2, v4, v2
	v_add_u32_e32 v7, 0xff, v7
	v_ashrrev_i32_e32 v6, 8, v6
	s_and_b64 s[4:5], vcc, s[8:9]
	v_cmp_lt_i32_e32 vcc, s34, v2
	v_cmp_ge_i32_e64 s[8:9], s34, v2
	v_add_u32_e32 v2, v5, v2
	v_ashrrev_i32_e32 v7, 8, v7
	v_cndmask_b32_e64 v3, 0, 1, s[4:5]
	s_and_b64 s[4:5], s[10:11], vcc
	v_cmp_lt_i32_e32 vcc, s34, v2
	v_cmp_ge_i32_e64 s[10:11], s34, v2
	v_add_u32_e32 v2, v6, v2
	v_cndmask_b32_e64 v3, v3, 2, s[4:5]
	s_and_b64 s[4:5], s[8:9], vcc
	v_cmp_lt_i32_e32 vcc, s34, v2
	v_cmp_ge_i32_e64 s[8:9], s34, v2
	v_add_u32_e32 v2, v7, v2
	v_add_u32_e32 v4, 0xff, v8
	v_cndmask_b32_e64 v3, v3, 3, s[4:5]
	s_and_b64 s[4:5], s[10:11], vcc
	v_cmp_lt_i32_e32 vcc, s34, v2
	v_ashrrev_i32_e32 v4, 8, v4
	v_cndmask_b32_e64 v3, v3, 4, s[4:5]
	s_and_b64 s[4:5], s[8:9], vcc
	v_cmp_ge_i32_e32 vcc, s34, v2
	v_add_u32_e32 v2, v4, v2
	v_add_u32_e32 v4, 0xff, v9
	v_cmp_lt_i32_e64 s[8:9], s34, v2
	v_ashrrev_i32_e32 v4, 8, v4
	v_cndmask_b32_e64 v3, v3, 5, s[4:5]
	s_and_b64 s[4:5], vcc, s[8:9]
	v_cmp_ge_i32_e32 vcc, s34, v2
	v_add_u32_e32 v2, v4, v2
	v_add_u32_e32 v4, 0xff, v14
	v_cmp_lt_i32_e64 s[8:9], s34, v2
	v_ashrrev_i32_e32 v4, 8, v4
	v_cndmask_b32_e64 v3, v3, 6, s[4:5]
	s_and_b64 s[4:5], vcc, s[8:9]
	v_cmp_ge_i32_e32 vcc, s34, v2
	v_add_u32_e32 v2, v4, v2
	v_add_u32_e32 v4, 0xff, v15
	v_cmp_lt_i32_e64 s[8:9], s34, v2
	v_ashrrev_i32_e32 v4, 8, v4
	v_cndmask_b32_e64 v3, v3, 7, s[4:5]
	s_and_b64 s[4:5], vcc, s[8:9]
	v_cmp_ge_i32_e32 vcc, s34, v2
	v_add_u32_e32 v2, v4, v2
	v_add_u32_e32 v4, 0xff, v16
	v_cmp_lt_i32_e64 s[8:9], s34, v2
	v_ashrrev_i32_e32 v4, 8, v4
	v_cndmask_b32_e64 v3, v3, 8, s[4:5]
	s_and_b64 s[4:5], vcc, s[8:9]
	v_cmp_ge_i32_e32 vcc, s34, v2
	v_add_u32_e32 v2, v4, v2
	v_add_u32_e32 v4, 0xff, v17
	v_cmp_lt_i32_e64 s[8:9], s34, v2
	v_ashrrev_i32_e32 v4, 8, v4
	v_cndmask_b32_e64 v3, v3, 9, s[4:5]
	s_and_b64 s[4:5], vcc, s[8:9]
	v_cmp_ge_i32_e32 vcc, s34, v2
	v_add_u32_e32 v2, v4, v2
	v_cmp_lt_i32_e64 s[8:9], s34, v2
	v_cndmask_b32_e64 v3, v3, 10, s[4:5]
	s_and_b64 s[4:5], vcc, s[8:9]
	v_cndmask_b32_e64 v14, v3, 11, s[4:5]
	v_add_u32_e32 v3, 0xff, v10
	v_ashrrev_i32_e32 v3, 8, v3
	v_cmp_ge_i32_e32 vcc, s34, v2
	v_add_u32_e32 v10, v3, v2
	ds_read_b128 v[2:5], v182 offset:112
	ds_read_b128 v[6:9], v182 offset:96
	v_cmp_lt_i32_e64 s[8:9], s34, v10
	v_ashrrev_i32_e32 v11, 8, v11
	s_and_b64 s[4:5], vcc, s[8:9]
	v_cmp_ge_i32_e32 vcc, s34, v10
	v_add_u32_e32 v10, v11, v10
	v_add_u32_e32 v12, 0xff, v12
	v_cmp_lt_i32_e64 s[8:9], s34, v10
	v_ashrrev_i32_e32 v12, 8, v12
	v_cndmask_b32_e64 v14, v14, 12, s[4:5]
	s_and_b64 s[4:5], vcc, s[8:9]
	v_cmp_ge_i32_e32 vcc, s34, v10
	v_add_u32_e32 v10, v12, v10
	v_add_u32_e32 v12, 0xff, v13
	v_cmp_lt_i32_e64 s[8:9], s34, v10
	v_ashrrev_i32_e32 v12, 8, v12
	v_cndmask_b32_e64 v11, v14, 13, s[4:5]
	s_and_b64 s[4:5], vcc, s[8:9]
	v_cmp_ge_i32_e32 vcc, s34, v10
	v_add_u32_e32 v10, v12, v10
	v_add_u32_e32 v12, 0xff, v22
	v_cmp_lt_i32_e64 s[8:9], s34, v10
	v_ashrrev_i32_e32 v12, 8, v12
	v_cndmask_b32_e64 v11, v11, 14, s[4:5]
	s_and_b64 s[4:5], vcc, s[8:9]
	v_cmp_ge_i32_e32 vcc, s34, v10
	v_add_u32_e32 v10, v12, v10
	v_add_u32_e32 v12, 0xff, v23
	v_cmp_lt_i32_e64 s[8:9], s34, v10
	v_ashrrev_i32_e32 v12, 8, v12
	v_cndmask_b32_e64 v11, v11, 15, s[4:5]
	s_and_b64 s[4:5], vcc, s[8:9]
	v_cmp_ge_i32_e32 vcc, s34, v10
	v_add_u32_e32 v10, v12, v10
	v_add_u32_e32 v12, 0xff, v24
	v_cmp_lt_i32_e64 s[8:9], s34, v10
	v_ashrrev_i32_e32 v12, 8, v12
	v_cndmask_b32_e64 v11, v11, 16, s[4:5]
	s_and_b64 s[4:5], vcc, s[8:9]
	v_cmp_ge_i32_e32 vcc, s34, v10
	v_add_u32_e32 v10, v12, v10
	v_add_u32_e32 v12, 0xff, v25
	v_cmp_lt_i32_e64 s[8:9], s34, v10
	v_ashrrev_i32_e32 v12, 8, v12
	v_cndmask_b32_e64 v11, v11, 17, s[4:5]
	s_and_b64 s[4:5], vcc, s[8:9]
	v_cmp_ge_i32_e32 vcc, s34, v10
	v_add_u32_e32 v10, v12, v10
	v_add_u32_e32 v12, 0xff, v18
	v_cmp_lt_i32_e64 s[8:9], s34, v10
	v_ashrrev_i32_e32 v12, 8, v12
	v_cndmask_b32_e64 v11, v11, 18, s[4:5]
	s_and_b64 s[4:5], vcc, s[8:9]
	v_cmp_ge_i32_e32 vcc, s34, v10
	v_add_u32_e32 v10, v12, v10
	v_add_u32_e32 v12, 0xff, v19
	v_cmp_lt_i32_e64 s[8:9], s34, v10
	v_ashrrev_i32_e32 v12, 8, v12
	v_cndmask_b32_e64 v11, v11, 19, s[4:5]
	s_and_b64 s[4:5], vcc, s[8:9]
	v_cmp_ge_i32_e32 vcc, s34, v10
	v_add_u32_e32 v10, v12, v10
	v_add_u32_e32 v12, 0xff, v20
	v_cmp_lt_i32_e64 s[8:9], s34, v10
	v_ashrrev_i32_e32 v12, 8, v12
	v_cndmask_b32_e64 v11, v11, 20, s[4:5]
	s_and_b64 s[4:5], vcc, s[8:9]
	v_cmp_ge_i32_e32 vcc, s34, v10
	v_add_u32_e32 v10, v12, v10
	v_add_u32_e32 v12, 0xff, v21
	v_cmp_lt_i32_e64 s[8:9], s34, v10
	v_ashrrev_i32_e32 v12, 8, v12
	v_cndmask_b32_e64 v11, v11, 21, s[4:5]
	s_and_b64 s[4:5], vcc, s[8:9]
	v_cmp_ge_i32_e32 vcc, s34, v10
	v_add_u32_e32 v10, v12, v10
	v_cmp_lt_i32_e64 s[8:9], s34, v10
	v_cndmask_b32_e64 v11, v11, 22, s[4:5]
	s_and_b64 s[4:5], vcc, s[8:9]
	v_cmp_ge_i32_e32 vcc, s34, v10
	s_waitcnt lgkmcnt(0)
	v_add_u32_e32 v6, 0xff, v6
	v_ashrrev_i32_e32 v6, 8, v6
	v_add_u32_e32 v6, v6, v10
	v_add_u32_e32 v7, 0xff, v7
	v_cmp_lt_i32_e64 s[8:9], s34, v6
	v_ashrrev_i32_e32 v7, 8, v7
	v_cndmask_b32_e64 v11, v11, 23, s[4:5]
	s_and_b64 s[4:5], vcc, s[8:9]
	v_cmp_ge_i32_e32 vcc, s34, v6
	v_add_u32_e32 v6, v7, v6
	v_add_u32_e32 v8, 0xff, v8
	v_cmp_lt_i32_e64 s[8:9], s34, v6
	v_ashrrev_i32_e32 v8, 8, v8
	v_cndmask_b32_e64 v10, v11, 24, s[4:5]
	s_and_b64 s[4:5], vcc, s[8:9]
	v_cmp_ge_i32_e32 vcc, s34, v6
	v_add_u32_e32 v6, v8, v6
	v_add_u32_e32 v8, 0xff, v9
	v_cmp_lt_i32_e64 s[8:9], s34, v6
	v_ashrrev_i32_e32 v8, 8, v8
	v_add_u32_e32 v2, 0xff, v2
	v_cndmask_b32_e64 v7, v10, 25, s[4:5]
	s_and_b64 s[4:5], vcc, s[8:9]
	v_cmp_ge_i32_e32 vcc, s34, v6
	v_add_u32_e32 v6, v8, v6
	v_ashrrev_i32_e32 v2, 8, v2
	v_cmp_lt_i32_e64 s[8:9], s34, v6
	v_add_u32_e32 v2, v2, v6
	v_add_u32_e32 v3, 0xff, v3
	v_cndmask_b32_e64 v7, v7, 26, s[4:5]
	s_and_b64 s[4:5], vcc, s[8:9]
	v_cmp_ge_i32_e32 vcc, s34, v6
	v_cmp_lt_i32_e64 s[8:9], s34, v2
	v_ashrrev_i32_e32 v3, 8, v3
	v_cndmask_b32_e64 v7, v7, 27, s[4:5]
	s_and_b64 s[4:5], vcc, s[8:9]
	v_cmp_ge_i32_e32 vcc, s34, v2
	v_add_u32_e32 v2, v3, v2
	v_add_u32_e32 v4, 0xff, v4
	v_cmp_lt_i32_e64 s[8:9], s34, v2
	v_ashrrev_i32_e32 v4, 8, v4
	v_cndmask_b32_e64 v6, v7, 28, s[4:5]
	s_and_b64 s[4:5], vcc, s[8:9]
	v_cmp_ge_i32_e32 vcc, s34, v2
	v_add_u32_e32 v2, v4, v2
	v_add_u32_e32 v4, 0xff, v5
	v_cmp_lt_i32_e64 s[8:9], s34, v2
	v_ashrrev_i32_e32 v4, 8, v4
	v_cndmask_b32_e64 v3, v6, 29, s[4:5]
	s_and_b64 s[4:5], vcc, s[8:9]
	v_cmp_ge_i32_e32 vcc, s34, v2
	v_add_u32_e32 v2, v4, v2
	v_cmp_lt_i32_e64 s[8:9], s34, v2
	v_cndmask_b32_e64 v3, v3, 30, s[4:5]
	s_and_b64 s[4:5], vcc, s[8:9]
	v_cndmask_b32_e64 v2, v3, 31, s[4:5]
	s_nop 0
	v_readfirstlane_b32 s8, v2
.LBB0_992:
	s_ashr_i32 s35, s34, 31
	s_lshl_b64 s[4:5], s[34:35], 19
	s_add_u32 s10, s47, s4
	s_addc_u32 s11, s48, s5
	s_and_b64 s[4:5], s[6:7], exec
	s_cselect_b32 s4, s11, s41
	s_cselect_b32 s5, s10, s40
	s_ashr_i32 s9, s8, 31
	s_ashr_i32 s31, s30, 31
	s_lshl_b64 s[38:39], s[30:31], 19
	s_lshl_b64 s[44:45], s[8:9], 22
	s_add_u32 s9, s3, s44
	s_addc_u32 s31, s19, s45
	s_add_u32 s38, s9, s38
	s_addc_u32 s39, s31, s39
	s_and_b64 s[44:45], s[6:7], exec
	s_cselect_b32 s9, s39, s43
	s_cselect_b32 s31, s38, s42
	s_add_u32 s40, s40, 0x80
	s_addc_u32 s41, s41, 0
	s_add_u32 s35, s42, 0x100
	v_mov_b32_e32 v34, 0
	s_addc_u32 s37, s43, 0
	s_mov_b32 s61, -2
	v_mov_b32_e32 v35, v34
	v_mov_b32_e32 v36, v34
	v_mov_b32_e32 v37, v34
	v_mov_b32_e32 v38, v34
	v_mov_b32_e32 v39, v34
	v_mov_b32_e32 v40, v34
	v_mov_b32_e32 v41, v34
	v_mov_b32_e32 v46, v34
	v_mov_b32_e32 v47, v34
	v_mov_b32_e32 v48, v34
	v_mov_b32_e32 v49, v34
	v_mov_b32_e32 v54, v34
	v_mov_b32_e32 v55, v34
	v_mov_b32_e32 v56, v34
	v_mov_b32_e32 v57, v34
	v_mov_b32_e32 v62, v34
	v_mov_b32_e32 v63, v34
	v_mov_b32_e32 v64, v34
	v_mov_b32_e32 v65, v34
	v_mov_b32_e32 v70, v34
	v_mov_b32_e32 v71, v34
	v_mov_b32_e32 v72, v34
	v_mov_b32_e32 v73, v34
	v_mov_b32_e32 v78, v34
	v_mov_b32_e32 v79, v34
	v_mov_b32_e32 v80, v34
	v_mov_b32_e32 v81, v34
	v_mov_b32_e32 v86, v34
	v_mov_b32_e32 v87, v34
	v_mov_b32_e32 v88, v34
	v_mov_b32_e32 v89, v34
	v_mov_b32_e32 v42, v34
	v_mov_b32_e32 v43, v34
	v_mov_b32_e32 v44, v34
	v_mov_b32_e32 v45, v34
	v_mov_b32_e32 v50, v34
	v_mov_b32_e32 v51, v34
	v_mov_b32_e32 v52, v34
	v_mov_b32_e32 v53, v34
	v_mov_b32_e32 v58, v34
	v_mov_b32_e32 v59, v34
	v_mov_b32_e32 v60, v34
	v_mov_b32_e32 v61, v34
	v_mov_b32_e32 v66, v34
	v_mov_b32_e32 v67, v34
	v_mov_b32_e32 v68, v34
	v_mov_b32_e32 v69, v34
	v_mov_b32_e32 v74, v34
	v_mov_b32_e32 v75, v34
	v_mov_b32_e32 v76, v34
	v_mov_b32_e32 v77, v34
	v_mov_b32_e32 v82, v34
	v_mov_b32_e32 v83, v34
	v_mov_b32_e32 v84, v34
	v_mov_b32_e32 v85, v34
	v_mov_b32_e32 v90, v34
	v_mov_b32_e32 v91, v34
	v_mov_b32_e32 v92, v34
	v_mov_b32_e32 v93, v34
	v_mov_b32_e32 v94, v34
	v_mov_b32_e32 v95, v34
	v_mov_b32_e32 v96, v34
	v_mov_b32_e32 v97, v34
	v_mov_b32_e32 v98, v34
	v_mov_b32_e32 v99, v34
	v_mov_b32_e32 v100, v34
	v_mov_b32_e32 v101, v34
	v_mov_b32_e32 v102, v34
	v_mov_b32_e32 v103, v34
	v_mov_b32_e32 v104, v34
	v_mov_b32_e32 v105, v34
	v_mov_b32_e32 v114, v34
	v_mov_b32_e32 v115, v34
	v_mov_b32_e32 v116, v34
	v_mov_b32_e32 v117, v34
	v_mov_b32_e32 v118, v34
	v_mov_b32_e32 v119, v34
	v_mov_b32_e32 v120, v34
	v_mov_b32_e32 v121, v34
	v_mov_b32_e32 v122, v34
	v_mov_b32_e32 v123, v34
	v_mov_b32_e32 v124, v34
	v_mov_b32_e32 v125, v34
	v_mov_b32_e32 v126, v34
	v_mov_b32_e32 v127, v34
	v_mov_b32_e32 v128, v34
	v_mov_b32_e32 v129, v34
	v_mov_b32_e32 v130, v34
	v_mov_b32_e32 v131, v34
	v_mov_b32_e32 v132, v34
	v_mov_b32_e32 v133, v34
	v_mov_b32_e32 v138, v34
	v_mov_b32_e32 v139, v34
	v_mov_b32_e32 v140, v34
	v_mov_b32_e32 v141, v34
	v_mov_b32_e32 v106, v34
	v_mov_b32_e32 v107, v34
	v_mov_b32_e32 v108, v34
	v_mov_b32_e32 v109, v34
	v_mov_b32_e32 v110, v34
	v_mov_b32_e32 v111, v34
	v_mov_b32_e32 v112, v34
	v_mov_b32_e32 v113, v34
	v_mov_b32_e32 v134, v34
	v_mov_b32_e32 v135, v34
	v_mov_b32_e32 v136, v34
	v_mov_b32_e32 v137, v34
	v_mov_b32_e32 v142, v34
	v_mov_b32_e32 v143, v34
	v_mov_b32_e32 v144, v34
	v_mov_b32_e32 v145, v34
	v_mov_b32_e32 v146, v34
	v_mov_b32_e32 v147, v34
	v_mov_b32_e32 v148, v34
	v_mov_b32_e32 v149, v34
	v_mov_b32_e32 v150, v34
	v_mov_b32_e32 v151, v34
	v_mov_b32_e32 v152, v34
	v_mov_b32_e32 v153, v34
	v_mov_b32_e32 v154, v34
	v_mov_b32_e32 v155, v34
	v_mov_b32_e32 v156, v34
	v_mov_b32_e32 v157, v34
	v_mov_b32_e32 v158, v34
	v_mov_b32_e32 v159, v34
	v_mov_b32_e32 v160, v34
	v_mov_b32_e32 v161, v34
	v_readlane_b32 s42, v255, 31
	s_xor_b32 s42, s42, 1
	s_and_b32 s42, s42, 1
	v_writelane_b32 v255, s42, 31
	s_lshl_b32 s42, s42, 10
	s_add_u32 m0, s42, 0x20000
	s_lshl_b32 s44, s36, 13
	s_lshl_b32 s45, s24, 10
	s_add_u32 s44, s44, s45
	s_add_u32 s44, s16, s44
	s_addc_u32 s45, s17, 0
	v_and_b32_e32 v2, 63, v0
	v_lshlrev_b32_e32 v2, 4, v2
	global_load_lds_dwordx4 v2, s[44:45]
	s_branch .LBB0_994

.LBB0_998:
	v_mov_b32_e32 v165, v0
	s_lshl_b32 s5, s24, 8
	v_readfirstlane_b32 s9, v165
	s_and_b32 s4, s9, 0xc0
	s_or_b32 s4, s4, s5
	s_ashr_i32 s37, s36, 31
	v_and_or_b32 v18, v165, 48, s4
	s_lshl_b64 s[4:5], s[36:37], 13
	s_add_u32 s4, s16, s4
	s_addc_u32 s5, s17, s5
	v_ashrrev_i32_e32 v19, 31, v18
	v_readlane_b32 s4, v255, 31
	s_and_b32 s4, s4, 1
	s_lshl_b32 s4, s4, 10
	s_add_u32 s4, s4, 0x20000
	v_lshlrev_b32_e32 v2, 2, v18
	v_and_b32_e32 v2, 0x3ff, v2
	v_add_u32_e32 v2, s4, v2
	ds_read_b128 v[14:17], v2
	ds_read_b128 v[10:13], v2 offset:16
	ds_read_b128 v[6:9], v2 offset:32
	ds_read_b128 v[2:5], v2 offset:48
	v_mov_b32_e32 v20, v163
	v_mov_b32_e32 v21, v163
	v_mov_b32_e32 v22, v163
	v_mov_b32_e32 v23, v163
	v_mov_b32_e32 v24, v163
	v_mov_b32_e32 v25, v163
	v_mov_b32_e32 v26, v163
	v_mov_b32_e32 v27, v163
	v_mov_b32_e32 v28, v163
	v_mov_b32_e32 v29, v163
	v_mov_b32_e32 v30, v163
	v_mov_b32_e32 v31, v163
	s_ashr_i32 s4, s9, 2
	s_andn2_b32 s4, s4, 63
	v_lshl_add_u64 v[32:33], s[28:29], 0, v[18:19]
	v_and_or_b32 v18, v165, 15, s4
	v_lshl_add_u32 v184, s18, 8, v18
	v_ashrrev_i32_e32 v185, 31, v184
	v_or_b32_e32 v182, 16, v184
	v_or_b32_e32 v186, 32, v184
	v_lshlrev_b64 v[18:19], 11, v[184:185]
	v_ashrrev_i32_e32 v183, 31, v182
	v_ashrrev_i32_e32 v187, 31, v186
	v_mov_b32_e32 v180, v163
	v_lshl_add_u64 v[18:19], v[32:33], 0, v[18:19]
	v_lshlrev_b64 v[182:183], 11, v[182:183]
	v_lshlrev_b64 v[186:187], 11, v[186:187]
	v_lshl_add_u64 v[182:183], v[32:33], 0, v[182:183]
	v_lshl_add_u64 v[186:187], v[32:33], 0, v[186:187]
	v_mov_b32_e32 v181, v163
	s_mov_b64 s[4:5], -1
	s_waitcnt lgkmcnt(0)
	v_pk_add_f32 v[158:159], v[158:159], v[14:15]
	v_pk_add_f32 v[154:155], v[154:155], v[10:11]
	v_pk_add_f32 v[138:139], v[138:139], v[6:7]
	v_pk_add_f32 v[130:131], v[130:131], v[2:3]
	v_pk_add_f32 v[150:151], v[150:151], v[14:15]
	v_pk_add_f32 v[146:147], v[146:147], v[10:11]
	v_pk_add_f32 v[126:127], v[126:127], v[6:7]
	v_pk_add_f32 v[122:123], v[122:123], v[2:3]
	v_cvt_pk_fp8_f32 v20, v158, v159
	v_cvt_pk_fp8_f32 v21, v154, v155
	v_cvt_pk_fp8_f32 v22, v138, v139
	v_cvt_pk_fp8_f32 v23, v130, v131
	v_pk_add_f32 v[142:143], v[142:143], v[14:15]
	v_pk_add_f32 v[134:135], v[134:135], v[10:11]
	v_pk_add_f32 v[118:119], v[118:119], v[6:7]
	v_pk_add_f32 v[114:115], v[114:115], v[2:3]
	v_cvt_pk_fp8_f32 v24, v150, v151
	v_cvt_pk_fp8_f32 v25, v146, v147
	v_cvt_pk_fp8_f32 v26, v126, v127
	v_cvt_pk_fp8_f32 v27, v122, v123
	v_cvt_pk_fp8_f32 v28, v142, v143
	v_cvt_pk_fp8_f32 v29, v134, v135
	v_cvt_pk_fp8_f32 v30, v118, v119
	v_cvt_pk_fp8_f32 v31, v114, v115
	v_pk_add_f32 v[160:161], v[160:161], v[16:17]
	v_pk_add_f32 v[156:157], v[156:157], v[12:13]
	v_pk_add_f32 v[140:141], v[140:141], v[8:9]
	v_pk_add_f32 v[132:133], v[132:133], v[4:5]
	v_pk_add_f32 v[152:153], v[152:153], v[16:17]
	v_pk_add_f32 v[148:149], v[148:149], v[12:13]
	v_pk_add_f32 v[128:129], v[128:129], v[8:9]
	v_pk_add_f32 v[124:125], v[124:125], v[4:5]
	v_cvt_pk_fp8_f32 v20, v160, v161 op_sel:[0,0,1]
	v_cvt_pk_fp8_f32 v21, v156, v157 op_sel:[0,0,1]
	v_cvt_pk_fp8_f32 v22, v140, v141 op_sel:[0,0,1]
	v_cvt_pk_fp8_f32 v23, v132, v133 op_sel:[0,0,1]
	v_pk_add_f32 v[144:145], v[144:145], v[16:17]
	v_pk_add_f32 v[136:137], v[136:137], v[12:13]
	v_pk_add_f32 v[120:121], v[120:121], v[8:9]
	v_pk_add_f32 v[116:117], v[116:117], v[4:5]
	v_cvt_pk_fp8_f32 v24, v152, v153 op_sel:[0,0,1]
	v_cvt_pk_fp8_f32 v25, v148, v149 op_sel:[0,0,1]
	v_cvt_pk_fp8_f32 v26, v128, v129 op_sel:[0,0,1]
	v_cvt_pk_fp8_f32 v27, v124, v125 op_sel:[0,0,1]
	v_cvt_pk_fp8_f32 v28, v144, v145 op_sel:[0,0,1]
	v_cvt_pk_fp8_f32 v29, v136, v137 op_sel:[0,0,1]
	v_cvt_pk_fp8_f32 v30, v120, v121 op_sel:[0,0,1]
	v_cvt_pk_fp8_f32 v31, v116, v117 op_sel:[0,0,1]
	v_pk_add_f32 v[110:111], v[110:111], v[14:15]
	global_store_dwordx4 v[18:19], v[20:23], off
	global_store_dwordx4 v[182:183], v[24:27], off
	global_store_dwordx4 v[186:187], v[28:31], off
	v_cvt_pk_fp8_f32 v180, v110, v111
	v_pk_add_f32 v[20:21], v[106:107], v[10:11]
	v_mov_b32_e32 v182, v163
	v_cvt_pk_fp8_f32 v181, v20, v21
	v_pk_add_f32 v[20:21], v[112:113], v[16:17]
	v_mov_b32_e32 v183, v163
	v_cvt_pk_fp8_f32 v180, v20, v21 op_sel:[0,0,1]
	v_pk_add_f32 v[20:21], v[108:109], v[12:13]
	v_pk_add_f32 v[22:23], v[94:95], v[14:15]
	v_cvt_pk_fp8_f32 v181, v20, v21 op_sel:[0,0,1]
	v_pk_add_f32 v[20:21], v[102:103], v[6:7]
	v_pk_add_f32 v[24:25], v[86:87], v[6:7]
	v_cvt_pk_fp8_f32 v182, v20, v21
	v_pk_add_f32 v[20:21], v[98:99], v[2:3]
	s_nop 0
	v_cvt_pk_fp8_f32 v183, v20, v21
	v_pk_add_f32 v[20:21], v[104:105], v[8:9]
	s_nop 0
	v_cvt_pk_fp8_f32 v182, v20, v21 op_sel:[0,0,1]
	v_pk_add_f32 v[20:21], v[100:101], v[4:5]
	s_nop 0
	v_cvt_pk_fp8_f32 v183, v20, v21 op_sel:[0,0,1]
	v_or_b32_e32 v20, 48, v184
	v_ashrrev_i32_e32 v21, 31, v20
	v_lshlrev_b64 v[20:21], 11, v[20:21]
	v_lshl_add_u64 v[20:21], v[32:33], 0, v[20:21]
	global_store_dwordx4 v[20:21], v[180:183], off
	v_mov_b32_e32 v20, v163
	v_cvt_pk_fp8_f32 v20, v22, v23
	v_pk_add_f32 v[22:23], v[90:91], v[10:11]
	v_mov_b32_e32 v21, v163
	v_cvt_pk_fp8_f32 v21, v22, v23
	v_pk_add_f32 v[22:23], v[96:97], v[16:17]
	s_nop 0
	v_cvt_pk_fp8_f32 v20, v22, v23 op_sel:[0,0,1]
	v_pk_add_f32 v[22:23], v[92:93], v[12:13]
	s_nop 0
	v_cvt_pk_fp8_f32 v21, v22, v23 op_sel:[0,0,1]
	v_mov_b32_e32 v22, v163
	v_cvt_pk_fp8_f32 v22, v24, v25
	v_pk_add_f32 v[24:25], v[78:79], v[2:3]
	v_mov_b32_e32 v23, v163
	v_cvt_pk_fp8_f32 v23, v24, v25
	v_pk_add_f32 v[24:25], v[88:89], v[8:9]
	s_nop 0
	v_cvt_pk_fp8_f32 v22, v24, v25 op_sel:[0,0,1]
	v_pk_add_f32 v[24:25], v[80:81], v[4:5]
	s_nop 0
	v_cvt_pk_fp8_f32 v23, v24, v25 op_sel:[0,0,1]
	v_add_co_u32_e32 v24, vcc, s55, v18
	s_nop 1
	v_addc_co_u32_e32 v25, vcc, 0, v19, vcc
	global_store_dwordx4 v[24:25], v[20:23], off
	v_pk_add_f32 v[24:25], v[70:71], v[6:7]
	s_nop 0
	v_pk_add_f32 v[22:23], v[82:83], v[14:15]
	v_mov_b32_e32 v20, v163
	v_cvt_pk_fp8_f32 v20, v22, v23
	v_pk_add_f32 v[22:23], v[74:75], v[10:11]
	v_mov_b32_e32 v21, v163
	v_cvt_pk_fp8_f32 v21, v22, v23
	v_pk_add_f32 v[22:23], v[84:85], v[16:17]
	s_nop 0
	v_cvt_pk_fp8_f32 v20, v22, v23 op_sel:[0,0,1]
	v_pk_add_f32 v[22:23], v[76:77], v[12:13]
	s_nop 0
	v_cvt_pk_fp8_f32 v21, v22, v23 op_sel:[0,0,1]
	v_mov_b32_e32 v22, v163
	v_cvt_pk_fp8_f32 v22, v24, v25
	v_pk_add_f32 v[24:25], v[62:63], v[2:3]
	v_mov_b32_e32 v23, v163
	v_cvt_pk_fp8_f32 v23, v24, v25
	v_pk_add_f32 v[24:25], v[72:73], v[8:9]
	s_nop 0
	v_cvt_pk_fp8_f32 v22, v24, v25 op_sel:[0,0,1]
	v_pk_add_f32 v[24:25], v[64:65], v[4:5]
	s_nop 0
	v_cvt_pk_fp8_f32 v23, v24, v25 op_sel:[0,0,1]
	v_add_co_u32_e32 v24, vcc, s59, v18
	s_nop 1
	v_addc_co_u32_e32 v25, vcc, 0, v19, vcc
	global_store_dwordx4 v[24:25], v[20:23], off
	v_pk_add_f32 v[24:25], v[54:55], v[6:7]
	v_pk_add_f32 v[6:7], v[38:39], v[6:7]
	v_pk_add_f32 v[22:23], v[66:67], v[14:15]
	v_mov_b32_e32 v20, v163
	v_cvt_pk_fp8_f32 v20, v22, v23
	v_pk_add_f32 v[22:23], v[58:59], v[10:11]
	v_mov_b32_e32 v21, v163
	v_cvt_pk_fp8_f32 v21, v22, v23
	v_pk_add_f32 v[22:23], v[68:69], v[16:17]
	v_pk_add_f32 v[10:11], v[42:43], v[10:11]
	v_cvt_pk_fp8_f32 v20, v22, v23 op_sel:[0,0,1]
	v_pk_add_f32 v[22:23], v[60:61], v[12:13]
	s_nop 0
	v_cvt_pk_fp8_f32 v21, v22, v23 op_sel:[0,0,1]
	v_mov_b32_e32 v22, v163
	v_cvt_pk_fp8_f32 v22, v24, v25
	v_pk_add_f32 v[24:25], v[46:47], v[2:3]
	v_mov_b32_e32 v23, v163
	v_cvt_pk_fp8_f32 v23, v24, v25
	v_pk_add_f32 v[24:25], v[56:57], v[8:9]
	v_pk_add_f32 v[2:3], v[34:35], v[2:3]
	v_cvt_pk_fp8_f32 v22, v24, v25 op_sel:[0,0,1]
	v_pk_add_f32 v[24:25], v[48:49], v[4:5]
	s_nop 0
	v_cvt_pk_fp8_f32 v23, v24, v25 op_sel:[0,0,1]
	v_add_co_u32_e32 v24, vcc, s60, v18
	s_nop 1
	v_addc_co_u32_e32 v25, vcc, 0, v19, vcc
	global_store_dwordx4 v[24:25], v[20:23], off
	s_nop 1
	v_pk_add_f32 v[20:21], v[50:51], v[14:15]
	v_mov_b32_e32 v15, v163
	v_mov_b32_e32 v14, v163
	v_cvt_pk_fp8_f32 v15, v10, v11
	v_pk_add_f32 v[10:11], v[52:53], v[16:17]
	v_mov_b32_e32 v16, v163
	v_cvt_pk_fp8_f32 v14, v20, v21
	v_cvt_pk_fp8_f32 v16, v6, v7
	v_mov_b32_e32 v17, v163
	v_cvt_pk_fp8_f32 v17, v2, v3
	v_pk_add_f32 v[2:3], v[40:41], v[8:9]
	v_cvt_pk_fp8_f32 v14, v10, v11 op_sel:[0,0,1]
	v_pk_add_f32 v[10:11], v[44:45], v[12:13]
	v_cvt_pk_fp8_f32 v16, v2, v3 op_sel:[0,0,1]
	v_pk_add_f32 v[2:3], v[36:37], v[4:5]
	v_cvt_pk_fp8_f32 v15, v10, v11 op_sel:[0,0,1]
	v_cvt_pk_fp8_f32 v17, v2, v3 op_sel:[0,0,1]
	v_add_co_u32_e32 v2, vcc, 0x58000, v18
	s_nop 1
	v_addc_co_u32_e32 v3, vcc, 0, v19, vcc
	s_andn2_b64 vcc, exec, s[6:7]
	global_store_dwordx4 v[2:3], v[14:17], off
	s_cbranch_vccnz .LBB0_989
	s_andn2_b64 vcc, exec, s[20:21]
	s_cbranch_vccnz .LBB0_988
	s_barrier
	s_branch .LBB0_988
